# v14 = v13 + residual/gate GEMM epilogue de-waterfalled: 8 operand loads per row block issued together, counted vmcnt per group (out0, ffndn, out1)
# baseline (speedup 1.0000x reference)
;     __device__ __forceinline__ void operator()(const pg8::f32x4 (&acc)[2][2][4][2], const pg8::Unit& u, int wr, int wc, int fr, int fq) const {
;         const int row0 = u.pm * 256 + wr * 64 + fr, col0 = u.pn * 256 + wc * 32 + 4 * fq;
; #pragma unroll
;         for (int ai = 0; ai < 2; ++ai)
; #pragma unroll
;             for (int m = 0; m < 4; ++m) { const int row = row0 + ai * 128 + m * 16;
;                 const float* rp = (row < NL ? res_lat + (size_t)row * DM : res_ctx + (size_t)(row - NL) * DM) + col0;
;                 const float* gp = gate + rowgrp(row) * MODW + col0;
;                 float* cp = C + (size_t)row * DM + col0;
; #pragma unroll
;                 for (int bj = 0; bj < 2; ++bj)
; #pragma unroll
;                     for (int n = 0; n < 2; ++n) { const pg8::f32x4 r = *(const pg8::f32x4*)(rp + bj * 128 + n * 16), g = *(const pg8::f32x4*)(gp + bj * 128 + n * 16);
;                         *(pg8::f32x4*)(cp + bj * 128 + n * 16) = r + g * acc[ai][bj][m][n]; } }
;     }
.LBB0_899:
	s_or_b64 exec, exec, s[6:7]
	v_lshrrev_b32_e32 v134, 20, v147
	v_lshl_or_b32 v144, s24, 8, v154
	v_add_u32_e32 v134, v146, v134
	v_ashrrev_i32_e32 v145, 31, v144
	v_ashrrev_i32_e32 v134, 12, v134
	v_lshlrev_b64 v[144:145], 2, v[144:145]
	v_mul_i32_i24_e32 v134, 0x3000, v134
	v_lshl_add_u64 v[160:161], v[150:151], 0, v[144:145]
	v_cndmask_b32_e32 v150, v158, v134, vcc
	v_ashrrev_i32_e32 v151, 31, v150
	v_lshl_add_u64 v[150:151], v[150:151], 2, s[10:11]
	v_lshl_add_u64 v[174:175], v[150:151], 0, v[144:145]
	global_load_dwordx4 v[166:169], v[160:161], off
	global_load_dwordx4 v[170:173], v[174:175], off
	global_load_dwordx4 v[226:229], v[160:161], off offset:64
	global_load_dwordx4 v[230:233], v[174:175], off offset:64
	global_load_dwordx4 v[234:237], v[160:161], off offset:512
	global_load_dwordx4 v[238:241], v[174:175], off offset:512
	global_load_dwordx4 v[194:197], v[160:161], off offset:576
	global_load_dwordx4 v[198:201], v[174:175], off offset:576
	v_readlane_b32 s68, v248, 9
	v_readlane_b32 s70, v248, 11
	v_readlane_b32 s71, v248, 12
	v_readlane_b32 s69, v248, 10
	v_readlane_b32 s72, v248, 13
	v_lshl_add_u64 v[148:149], s[70:71], 0, v[148:149]
	v_lshl_add_u64 v[176:177], v[148:149], 0, v[144:145]
	v_readlane_b32 s73, v248, 14
	v_readlane_b32 s74, v248, 15
	v_readlane_b32 s75, v248, 16
	v_readlane_b32 s76, v248, 17
	v_readlane_b32 s77, v248, 18
	v_readlane_b32 s78, v248, 19
	v_readlane_b32 s79, v248, 20
	v_readlane_b32 s80, v248, 21
	v_readlane_b32 s81, v248, 22
	v_readlane_b32 s82, v248, 23
	v_readlane_b32 s83, v248, 24
	s_waitcnt vmcnt(6)
	v_pk_fma_f32 v[128:129], v[128:129], v[172:173], v[168:169]
	v_pk_fma_f32 v[126:127], v[126:127], v[170:171], v[166:167]
	global_store_dwordx4 v[176:177], v[126:129], off
	s_nop 1
	s_waitcnt vmcnt(5)
	v_pk_fma_f32 v[124:125], v[124:125], v[232:233], v[228:229]
	v_pk_fma_f32 v[122:123], v[122:123], v[230:231], v[226:227]
	global_store_dwordx4 v[176:177], v[122:125], off offset:64
	s_nop 1
	s_waitcnt vmcnt(4)
	v_pk_fma_f32 v[120:121], v[120:121], v[240:241], v[236:237]
	v_pk_fma_f32 v[118:119], v[118:119], v[238:239], v[234:235]
	global_store_dwordx4 v[176:177], v[118:121], off offset:512
	s_nop 1
	v_or_b32_e32 v118, 16, v146
	v_cmp_gt_i32_e32 vcc, s33, v118
	v_cmp_lt_i32_e64 s[6:7], s41, v118
	s_waitcnt vmcnt(3)
	v_pk_fma_f32 v[116:117], v[116:117], v[200:201], v[196:197]
	v_pk_fma_f32 v[114:115], v[114:115], v[198:199], v[194:195]
	global_store_dwordx4 v[176:177], v[114:117], off offset:576
	s_and_saveexec_b64 s[26:27], s[6:7]
	s_xor_b64 s[6:7], exec, s[26:27]
	s_cbranch_execz .LBB0_901
	v_add_u32_e32 v134, 0xffffe010, v146
	v_readlane_b32 s68, v247, 35
	v_lshlrev_b64 v[114:115], 13, v[134:135]
	v_readlane_b32 s72, v247, 39
	v_readlane_b32 s73, v247, 40
	v_mov_b32_e32 v119, v135
	v_readlane_b32 s69, v247, 36
	v_lshl_add_u64 v[116:117], s[72:73], 0, v[114:115]
	v_lshlrev_b64 v[114:115], 13, v[118:119]
	v_readlane_b32 s70, v247, 37
	v_readlane_b32 s71, v247, 38
	v_readlane_b32 s74, v247, 41
	v_readlane_b32 s75, v247, 42
	v_readlane_b32 s76, v247, 43
	v_readlane_b32 s77, v247, 44
	v_readlane_b32 s78, v247, 45
	v_readlane_b32 s79, v247, 46
	v_readlane_b32 s80, v247, 47
	v_readlane_b32 s81, v247, 48
	v_readlane_b32 s82, v247, 49
	v_readlane_b32 s83, v247, 50

;     __device__ __forceinline__ void operator()(const pg8::f32x4 (&acc)[2][2][4][2], const pg8::Unit& u, int wr, int wc, int fr, int fq) const {
;         const int row0 = u.pm * 256 + wr * 64 + fr, col0 = u.pn * 256 + wc * 32 + 4 * fq;
; #pragma unroll
;         for (int ai = 0; ai < 2; ++ai)
; #pragma unroll
;             for (int m = 0; m < 4; ++m) { const int row = row0 + ai * 128 + m * 16;
;                 const float* rp = (row < NL ? res_lat + (size_t)row * DM : res_ctx + (size_t)(row - NL) * DM) + col0;
;                 const float* gp = gate + rowgrp(row) * MODW + col0;
;                 float* cp = C + (size_t)row * DM + col0;
; #pragma unroll
;                 for (int bj = 0; bj < 2; ++bj)
; #pragma unroll
;                     for (int n = 0; n < 2; ++n) { const pg8::f32x4 r = *(const pg8::f32x4*)(rp + bj * 128 + n * 16), g = *(const pg8::f32x4*)(gp + bj * 128 + n * 16);
;                         *(pg8::f32x4*)(cp + bj * 128 + n * 16) = r + g * acc[ai][bj][m][n]; } }
;     }
.LBB0_903:
	s_or_b64 exec, exec, s[6:7]
	v_lshl_add_u64 v[124:125], v[116:117], 0, v[144:145]
	v_lshrrev_b32_e32 v116, 20, v119
	v_add_u32_e32 v116, v118, v116
	v_ashrrev_i32_e32 v116, 12, v116
	v_mul_i32_i24_e32 v116, 0x3000, v116
	v_cndmask_b32_e32 v116, v158, v116, vcc
	v_ashrrev_i32_e32 v117, 31, v116
	v_lshl_add_u64 v[116:117], v[116:117], 2, s[10:11]
	v_lshl_add_u64 v[126:127], v[116:117], 0, v[144:145]
	global_load_dwordx4 v[116:119], v[124:125], off
	global_load_dwordx4 v[120:123], v[126:127], off
	global_load_dwordx4 v[226:229], v[124:125], off offset:64
	global_load_dwordx4 v[230:233], v[126:127], off offset:64
	global_load_dwordx4 v[234:237], v[124:125], off offset:512
	global_load_dwordx4 v[238:241], v[126:127], off offset:512
	global_load_dwordx4 v[194:197], v[124:125], off offset:576
	global_load_dwordx4 v[198:201], v[126:127], off offset:576
	v_readlane_b32 s68, v248, 9
	v_readlane_b32 s70, v248, 11
	v_readlane_b32 s71, v248, 12
	v_readlane_b32 s69, v248, 10
	v_readlane_b32 s72, v248, 13
	v_lshl_add_u64 v[114:115], s[70:71], 0, v[114:115]
	v_lshl_add_u64 v[128:129], v[114:115], 0, v[144:145]
	v_readlane_b32 s73, v248, 14
	v_readlane_b32 s74, v248, 15
	v_readlane_b32 s75, v248, 16
	v_readlane_b32 s76, v248, 17
	v_readlane_b32 s77, v248, 18
	v_readlane_b32 s78, v248, 19
	v_readlane_b32 s79, v248, 20
	v_readlane_b32 s80, v248, 21
	v_readlane_b32 s81, v248, 22
	v_readlane_b32 s82, v248, 23
	v_readlane_b32 s83, v248, 24
	s_waitcnt vmcnt(6)
	v_pk_fma_f32 v[112:113], v[112:113], v[122:123], v[118:119]
	v_pk_fma_f32 v[110:111], v[110:111], v[120:121], v[116:117]
	global_store_dwordx4 v[128:129], v[110:113], off
	s_nop 1
	s_waitcnt vmcnt(5)
	v_pk_fma_f32 v[108:109], v[108:109], v[232:233], v[228:229]
	v_pk_fma_f32 v[106:107], v[106:107], v[230:231], v[226:227]
	global_store_dwordx4 v[128:129], v[106:109], off offset:64
	s_nop 1
	s_waitcnt vmcnt(4)
	v_pk_fma_f32 v[104:105], v[104:105], v[240:241], v[236:237]
	v_pk_fma_f32 v[102:103], v[102:103], v[238:239], v[234:235]
	global_store_dwordx4 v[128:129], v[102:105], off offset:512
	s_nop 1
	v_or_b32_e32 v102, 32, v146
	v_cmp_gt_i32_e32 vcc, s33, v102
	v_cmp_lt_i32_e64 s[6:7], s41, v102
	s_waitcnt vmcnt(3)
	v_pk_fma_f32 v[100:101], v[100:101], v[200:201], v[196:197]
	v_pk_fma_f32 v[98:99], v[98:99], v[198:199], v[194:195]
	global_store_dwordx4 v[128:129], v[98:101], off offset:576
	s_and_saveexec_b64 s[26:27], s[6:7]
	s_xor_b64 s[6:7], exec, s[26:27]
	s_cbranch_execz .LBB0_905
	v_add_u32_e32 v134, 0xffffe020, v146
	v_readlane_b32 s68, v247, 35
	v_lshlrev_b64 v[98:99], 13, v[134:135]
	v_readlane_b32 s72, v247, 39
	v_readlane_b32 s73, v247, 40
	v_mov_b32_e32 v103, v135
	v_readlane_b32 s69, v247, 36
	v_lshl_add_u64 v[100:101], s[72:73], 0, v[98:99]
	v_lshlrev_b64 v[98:99], 13, v[102:103]
	v_readlane_b32 s70, v247, 37
	v_readlane_b32 s71, v247, 38
	v_readlane_b32 s74, v247, 41
	v_readlane_b32 s75, v247, 42
	v_readlane_b32 s76, v247, 43
	v_readlane_b32 s77, v247, 44
	v_readlane_b32 s78, v247, 45
	v_readlane_b32 s79, v247, 46
	v_readlane_b32 s80, v247, 47
	v_readlane_b32 s81, v247, 48
	v_readlane_b32 s82, v247, 49
	v_readlane_b32 s83, v247, 50

;     __device__ __forceinline__ void operator()(const pg8::f32x4 (&acc)[2][2][4][2], const pg8::Unit& u, int wr, int wc, int fr, int fq) const {
;         const int row0 = u.pm * 256 + wr * 64 + fr, col0 = u.pn * 256 + wc * 32 + 4 * fq;
; #pragma unroll
;         for (int ai = 0; ai < 2; ++ai)
; #pragma unroll
;             for (int m = 0; m < 4; ++m) { const int row = row0 + ai * 128 + m * 16;
;                 const float* rp = (row < NL ? res_lat + (size_t)row * DM : res_ctx + (size_t)(row - NL) * DM) + col0;
;                 const float* gp = gate + rowgrp(row) * MODW + col0;
;                 float* cp = C + (size_t)row * DM + col0;
; #pragma unroll
;                 for (int bj = 0; bj < 2; ++bj)
; #pragma unroll
;                     for (int n = 0; n < 2; ++n) { const pg8::f32x4 r = *(const pg8::f32x4*)(rp + bj * 128 + n * 16), g = *(const pg8::f32x4*)(gp + bj * 128 + n * 16);
;                         *(pg8::f32x4*)(cp + bj * 128 + n * 16) = r + g * acc[ai][bj][m][n]; } }
;     }
.LBB0_907:
	s_or_b64 exec, exec, s[6:7]
	v_lshl_add_u64 v[108:109], v[100:101], 0, v[144:145]
	v_lshrrev_b32_e32 v100, 20, v103
	v_add_u32_e32 v100, v102, v100
	v_ashrrev_i32_e32 v100, 12, v100
	v_mul_i32_i24_e32 v100, 0x3000, v100
	v_cndmask_b32_e32 v100, v158, v100, vcc
	v_ashrrev_i32_e32 v101, 31, v100
	v_lshl_add_u64 v[100:101], v[100:101], 2, s[10:11]
	v_lshl_add_u64 v[110:111], v[100:101], 0, v[144:145]
	global_load_dwordx4 v[100:103], v[108:109], off
	global_load_dwordx4 v[104:107], v[110:111], off
	global_load_dwordx4 v[226:229], v[108:109], off offset:64
	global_load_dwordx4 v[230:233], v[110:111], off offset:64
	global_load_dwordx4 v[234:237], v[108:109], off offset:512
	global_load_dwordx4 v[238:241], v[110:111], off offset:512
	global_load_dwordx4 v[194:197], v[108:109], off offset:576
	global_load_dwordx4 v[198:201], v[110:111], off offset:576
	v_readlane_b32 s68, v248, 9
	v_readlane_b32 s70, v248, 11
	v_readlane_b32 s71, v248, 12
	v_readlane_b32 s69, v248, 10
	v_readlane_b32 s72, v248, 13
	v_lshl_add_u64 v[98:99], s[70:71], 0, v[98:99]
	v_lshl_add_u64 v[112:113], v[98:99], 0, v[144:145]
	v_readlane_b32 s73, v248, 14
	v_readlane_b32 s74, v248, 15
	v_readlane_b32 s75, v248, 16
	v_readlane_b32 s76, v248, 17
	v_readlane_b32 s77, v248, 18
	v_readlane_b32 s78, v248, 19
	v_readlane_b32 s79, v248, 20
	v_readlane_b32 s80, v248, 21
	v_readlane_b32 s81, v248, 22
	v_readlane_b32 s82, v248, 23
	v_readlane_b32 s83, v248, 24
	s_waitcnt vmcnt(6)
	v_pk_fma_f32 v[96:97], v[96:97], v[106:107], v[102:103]
	v_pk_fma_f32 v[94:95], v[94:95], v[104:105], v[100:101]
	global_store_dwordx4 v[112:113], v[94:97], off
	s_nop 1
	s_waitcnt vmcnt(5)
	v_pk_fma_f32 v[92:93], v[92:93], v[232:233], v[228:229]
	v_pk_fma_f32 v[90:91], v[90:91], v[230:231], v[226:227]
	global_store_dwordx4 v[112:113], v[90:93], off offset:64
	s_nop 1
	s_waitcnt vmcnt(4)
	v_pk_fma_f32 v[88:89], v[88:89], v[240:241], v[236:237]
	v_pk_fma_f32 v[86:87], v[86:87], v[238:239], v[234:235]
	global_store_dwordx4 v[112:113], v[86:89], off offset:512
	s_nop 1
	v_or_b32_e32 v86, 48, v146
	v_cmp_gt_i32_e32 vcc, s33, v86
	v_cmp_lt_i32_e64 s[6:7], s41, v86
	s_waitcnt vmcnt(3)
	v_pk_fma_f32 v[84:85], v[84:85], v[200:201], v[196:197]
	v_pk_fma_f32 v[82:83], v[82:83], v[198:199], v[194:195]
	global_store_dwordx4 v[112:113], v[82:85], off offset:576
	s_and_saveexec_b64 s[26:27], s[6:7]
	s_xor_b64 s[6:7], exec, s[26:27]
	s_cbranch_execz .LBB0_909
	v_add_u32_e32 v134, 0xffffe030, v146
	v_readlane_b32 s68, v247, 35
	v_lshlrev_b64 v[82:83], 13, v[134:135]
	v_readlane_b32 s72, v247, 39
	v_readlane_b32 s73, v247, 40
	v_mov_b32_e32 v87, v135
	v_readlane_b32 s69, v247, 36
	v_lshl_add_u64 v[84:85], s[72:73], 0, v[82:83]
	v_lshlrev_b64 v[82:83], 13, v[86:87]
	v_readlane_b32 s70, v247, 37
	v_readlane_b32 s71, v247, 38
	v_readlane_b32 s74, v247, 41
	v_readlane_b32 s75, v247, 42
	v_readlane_b32 s76, v247, 43
	v_readlane_b32 s77, v247, 44
	v_readlane_b32 s78, v247, 45
	v_readlane_b32 s79, v247, 46
	v_readlane_b32 s80, v247, 47
	v_readlane_b32 s81, v247, 48
	v_readlane_b32 s82, v247, 49
	v_readlane_b32 s83, v247, 50

;     __device__ __forceinline__ void operator()(const pg8::f32x4 (&acc)[2][2][4][2], const pg8::Unit& u, int wr, int wc, int fr, int fq) const {
;         const int row0 = u.pm * 256 + wr * 64 + fr, col0 = u.pn * 256 + wc * 32 + 4 * fq;
; #pragma unroll
;         for (int ai = 0; ai < 2; ++ai)
; #pragma unroll
;             for (int m = 0; m < 4; ++m) { const int row = row0 + ai * 128 + m * 16;
;                 const float* rp = (row < NL ? res_lat + (size_t)row * DM : res_ctx + (size_t)(row - NL) * DM) + col0;
;                 const float* gp = gate + rowgrp(row) * MODW + col0;
;                 float* cp = C + (size_t)row * DM + col0;
; #pragma unroll
;                 for (int bj = 0; bj < 2; ++bj)
; #pragma unroll
;                     for (int n = 0; n < 2; ++n) { const pg8::f32x4 r = *(const pg8::f32x4*)(rp + bj * 128 + n * 16), g = *(const pg8::f32x4*)(gp + bj * 128 + n * 16);
;                         *(pg8::f32x4*)(cp + bj * 128 + n * 16) = r + g * acc[ai][bj][m][n]; } }
;     }
.LBB0_911:
	s_or_b64 exec, exec, s[6:7]
	v_lshl_add_u64 v[92:93], v[84:85], 0, v[144:145]
	v_lshrrev_b32_e32 v84, 20, v87
	v_add_u32_e32 v84, v86, v84
	v_ashrrev_i32_e32 v84, 12, v84
	v_mul_i32_i24_e32 v84, 0x3000, v84
	v_cndmask_b32_e32 v84, v158, v84, vcc
	v_ashrrev_i32_e32 v85, 31, v84
	v_lshl_add_u64 v[84:85], v[84:85], 2, s[10:11]
	v_lshl_add_u64 v[94:95], v[84:85], 0, v[144:145]
	global_load_dwordx4 v[84:87], v[92:93], off
	global_load_dwordx4 v[88:91], v[94:95], off
	global_load_dwordx4 v[226:229], v[92:93], off offset:64
	global_load_dwordx4 v[230:233], v[94:95], off offset:64
	global_load_dwordx4 v[234:237], v[92:93], off offset:512
	global_load_dwordx4 v[238:241], v[94:95], off offset:512
	global_load_dwordx4 v[194:197], v[92:93], off offset:576
	global_load_dwordx4 v[198:201], v[94:95], off offset:576
	v_readlane_b32 s68, v248, 9
	v_readlane_b32 s70, v248, 11
	v_readlane_b32 s71, v248, 12
	s_movk_i32 s6, 0x1f80
	v_cmp_gt_i32_e32 vcc, s6, v146
	v_lshl_add_u64 v[82:83], s[70:71], 0, v[82:83]
	v_lshl_add_u64 v[96:97], v[82:83], 0, v[144:145]
	s_movk_i32 s6, 0x1f7f
	v_cmp_lt_i32_e64 s[6:7], s6, v146
	v_readlane_b32 s69, v248, 10
	v_readlane_b32 s72, v248, 13
	v_readlane_b32 s73, v248, 14
	v_readlane_b32 s74, v248, 15
	v_readlane_b32 s75, v248, 16
	v_readlane_b32 s76, v248, 17
	v_readlane_b32 s77, v248, 18
	v_readlane_b32 s78, v248, 19
	v_readlane_b32 s79, v248, 20
	v_readlane_b32 s80, v248, 21
	v_readlane_b32 s81, v248, 22
	v_readlane_b32 s82, v248, 23
	v_readlane_b32 s83, v248, 24
	s_waitcnt vmcnt(6)
	v_pk_fma_f32 v[80:81], v[80:81], v[90:91], v[86:87]
	v_pk_fma_f32 v[78:79], v[78:79], v[88:89], v[84:85]
	global_store_dwordx4 v[96:97], v[78:81], off
	s_nop 1
	s_waitcnt vmcnt(5)
	v_pk_fma_f32 v[76:77], v[76:77], v[232:233], v[228:229]
	v_pk_fma_f32 v[74:75], v[74:75], v[230:231], v[226:227]
	global_store_dwordx4 v[96:97], v[74:77], off offset:64
	s_nop 1
	s_waitcnt vmcnt(4)
	v_pk_fma_f32 v[72:73], v[72:73], v[240:241], v[236:237]
	v_pk_fma_f32 v[70:71], v[70:71], v[238:239], v[234:235]
	global_store_dwordx4 v[96:97], v[70:73], off offset:512
	s_nop 1
	v_add_u32_e32 v70, 0x80, v146
	s_waitcnt vmcnt(3)
	v_pk_fma_f32 v[68:69], v[68:69], v[200:201], v[196:197]
	v_pk_fma_f32 v[66:67], v[66:67], v[198:199], v[194:195]
	global_store_dwordx4 v[96:97], v[66:69], off offset:576
	s_and_saveexec_b64 s[26:27], s[6:7]
	s_xor_b64 s[6:7], exec, s[26:27]
	s_cbranch_execz .LBB0_913
	v_add_u32_e32 v134, 0xffffe080, v146
	v_readlane_b32 s68, v247, 35
	v_lshlrev_b64 v[66:67], 13, v[134:135]
	v_readlane_b32 s72, v247, 39
	v_readlane_b32 s73, v247, 40
	v_mov_b32_e32 v71, v135
	v_readlane_b32 s69, v247, 36
	v_lshl_add_u64 v[68:69], s[72:73], 0, v[66:67]
	v_lshlrev_b64 v[66:67], 13, v[70:71]
	v_readlane_b32 s70, v247, 37
	v_readlane_b32 s71, v247, 38
	v_readlane_b32 s74, v247, 41
	v_readlane_b32 s75, v247, 42
	v_readlane_b32 s76, v247, 43
	v_readlane_b32 s77, v247, 44
	v_readlane_b32 s78, v247, 45
	v_readlane_b32 s79, v247, 46
	v_readlane_b32 s80, v247, 47
	v_readlane_b32 s81, v247, 48
	v_readlane_b32 s82, v247, 49
	v_readlane_b32 s83, v247, 50

;     __device__ __forceinline__ void operator()(const pg8::f32x4 (&acc)[2][2][4][2], const pg8::Unit& u, int wr, int wc, int fr, int fq) const {
;         const int row0 = u.pm * 256 + wr * 64 + fr, col0 = u.pn * 256 + wc * 32 + 4 * fq;
; #pragma unroll
;         for (int ai = 0; ai < 2; ++ai)
; #pragma unroll
;             for (int m = 0; m < 4; ++m) { const int row = row0 + ai * 128 + m * 16;
;                 const float* rp = (row < NL ? res_lat + (size_t)row * DM : res_ctx + (size_t)(row - NL) * DM) + col0;
;                 const float* gp = gate + rowgrp(row) * MODW + col0;
;                 float* cp = C + (size_t)row * DM + col0;
; #pragma unroll
;                 for (int bj = 0; bj < 2; ++bj)
; #pragma unroll
;                     for (int n = 0; n < 2; ++n) { const pg8::f32x4 r = *(const pg8::f32x4*)(rp + bj * 128 + n * 16), g = *(const pg8::f32x4*)(gp + bj * 128 + n * 16);
;                         *(pg8::f32x4*)(cp + bj * 128 + n * 16) = r + g * acc[ai][bj][m][n]; } }
;     }
.LBB0_915:
	s_or_b64 exec, exec, s[6:7]
	v_lshl_add_u64 v[76:77], v[68:69], 0, v[144:145]
	v_lshrrev_b32_e32 v68, 20, v71
	v_add_u32_e32 v68, v70, v68
	v_ashrrev_i32_e32 v68, 12, v68
	v_mul_i32_i24_e32 v68, 0x3000, v68
	v_cndmask_b32_e32 v68, v158, v68, vcc
	v_ashrrev_i32_e32 v69, 31, v68
	v_lshl_add_u64 v[68:69], v[68:69], 2, s[10:11]
	v_lshl_add_u64 v[78:79], v[68:69], 0, v[144:145]
	global_load_dwordx4 v[68:71], v[76:77], off
	global_load_dwordx4 v[72:75], v[78:79], off
	global_load_dwordx4 v[226:229], v[76:77], off offset:64
	global_load_dwordx4 v[230:233], v[78:79], off offset:64
	global_load_dwordx4 v[234:237], v[76:77], off offset:512
	global_load_dwordx4 v[238:241], v[78:79], off offset:512
	global_load_dwordx4 v[194:197], v[76:77], off offset:576
	global_load_dwordx4 v[198:201], v[78:79], off offset:576
	v_readlane_b32 s68, v248, 9
	v_readlane_b32 s70, v248, 11
	v_readlane_b32 s71, v248, 12
	s_movk_i32 s6, 0x1f70
	v_cmp_gt_i32_e32 vcc, s6, v146
	v_lshl_add_u64 v[66:67], s[70:71], 0, v[66:67]
	v_lshl_add_u64 v[80:81], v[66:67], 0, v[144:145]
	s_movk_i32 s6, 0x1f6f
	v_cmp_lt_i32_e64 s[6:7], s6, v146
	v_readlane_b32 s69, v248, 10
	v_readlane_b32 s72, v248, 13
	v_readlane_b32 s73, v248, 14
	v_readlane_b32 s74, v248, 15
	v_readlane_b32 s75, v248, 16
	v_readlane_b32 s76, v248, 17
	v_readlane_b32 s77, v248, 18
	v_readlane_b32 s78, v248, 19
	v_readlane_b32 s79, v248, 20
	v_readlane_b32 s80, v248, 21
	v_readlane_b32 s81, v248, 22
	v_readlane_b32 s82, v248, 23
	v_readlane_b32 s83, v248, 24
	s_waitcnt vmcnt(6)
	v_pk_fma_f32 v[64:65], v[64:65], v[74:75], v[70:71]
	v_pk_fma_f32 v[62:63], v[62:63], v[72:73], v[68:69]
	global_store_dwordx4 v[80:81], v[62:65], off
	s_nop 1
	s_waitcnt vmcnt(5)
	v_pk_fma_f32 v[60:61], v[60:61], v[232:233], v[228:229]
	v_pk_fma_f32 v[58:59], v[58:59], v[230:231], v[226:227]
	global_store_dwordx4 v[80:81], v[58:61], off offset:64
	s_nop 1
	s_waitcnt vmcnt(4)
	v_pk_fma_f32 v[56:57], v[56:57], v[240:241], v[236:237]
	v_pk_fma_f32 v[54:55], v[54:55], v[238:239], v[234:235]
	global_store_dwordx4 v[80:81], v[54:57], off offset:512
	s_nop 1
	v_add_u32_e32 v54, 0x90, v146
	s_waitcnt vmcnt(3)
	v_pk_fma_f32 v[52:53], v[52:53], v[200:201], v[196:197]
	v_pk_fma_f32 v[50:51], v[50:51], v[198:199], v[194:195]
	global_store_dwordx4 v[80:81], v[50:53], off offset:576
	s_and_saveexec_b64 s[26:27], s[6:7]
	s_xor_b64 s[6:7], exec, s[26:27]
	s_cbranch_execz .LBB0_917
	v_add_u32_e32 v134, 0xffffe090, v146
	v_readlane_b32 s68, v247, 35
	v_lshlrev_b64 v[50:51], 13, v[134:135]
	v_readlane_b32 s72, v247, 39
	v_readlane_b32 s73, v247, 40
	v_mov_b32_e32 v55, v135
	v_readlane_b32 s69, v247, 36
	v_lshl_add_u64 v[52:53], s[72:73], 0, v[50:51]
	v_lshlrev_b64 v[50:51], 13, v[54:55]
	v_readlane_b32 s70, v247, 37
	v_readlane_b32 s71, v247, 38
	v_readlane_b32 s74, v247, 41
	v_readlane_b32 s75, v247, 42
	v_readlane_b32 s76, v247, 43
	v_readlane_b32 s77, v247, 44
	v_readlane_b32 s78, v247, 45
	v_readlane_b32 s79, v247, 46
	v_readlane_b32 s80, v247, 47
	v_readlane_b32 s81, v247, 48
	v_readlane_b32 s82, v247, 49
	v_readlane_b32 s83, v247, 50

;     __device__ __forceinline__ void operator()(const pg8::f32x4 (&acc)[2][2][4][2], const pg8::Unit& u, int wr, int wc, int fr, int fq) const {
;         const int row0 = u.pm * 256 + wr * 64 + fr, col0 = u.pn * 256 + wc * 32 + 4 * fq;
; #pragma unroll
;         for (int ai = 0; ai < 2; ++ai)
; #pragma unroll
;             for (int m = 0; m < 4; ++m) { const int row = row0 + ai * 128 + m * 16;
;                 const float* rp = (row < NL ? res_lat + (size_t)row * DM : res_ctx + (size_t)(row - NL) * DM) + col0;
;                 const float* gp = gate + rowgrp(row) * MODW + col0;
;                 float* cp = C + (size_t)row * DM + col0;
; #pragma unroll
;                 for (int bj = 0; bj < 2; ++bj)
; #pragma unroll
;                     for (int n = 0; n < 2; ++n) { const pg8::f32x4 r = *(const pg8::f32x4*)(rp + bj * 128 + n * 16), g = *(const pg8::f32x4*)(gp + bj * 128 + n * 16);
;                         *(pg8::f32x4*)(cp + bj * 128 + n * 16) = r + g * acc[ai][bj][m][n]; } }
;     }
.LBB0_919:
	s_or_b64 exec, exec, s[6:7]
	v_lshl_add_u64 v[60:61], v[52:53], 0, v[144:145]
	v_lshrrev_b32_e32 v52, 20, v55
	v_add_u32_e32 v52, v54, v52
	v_ashrrev_i32_e32 v52, 12, v52
	v_mul_i32_i24_e32 v52, 0x3000, v52
	v_cndmask_b32_e32 v52, v158, v52, vcc
	v_ashrrev_i32_e32 v53, 31, v52
	v_lshl_add_u64 v[52:53], v[52:53], 2, s[10:11]
	v_lshl_add_u64 v[62:63], v[52:53], 0, v[144:145]
	global_load_dwordx4 v[52:55], v[60:61], off
	global_load_dwordx4 v[56:59], v[62:63], off
	global_load_dwordx4 v[226:229], v[60:61], off offset:64
	global_load_dwordx4 v[230:233], v[62:63], off offset:64
	global_load_dwordx4 v[234:237], v[60:61], off offset:512
	global_load_dwordx4 v[238:241], v[62:63], off offset:512
	global_load_dwordx4 v[194:197], v[60:61], off offset:576
	global_load_dwordx4 v[198:201], v[62:63], off offset:576
	v_readlane_b32 s68, v248, 9
	v_readlane_b32 s70, v248, 11
	v_readlane_b32 s71, v248, 12
	s_movk_i32 s6, 0x1f60
	v_cmp_gt_i32_e32 vcc, s6, v146
	v_lshl_add_u64 v[50:51], s[70:71], 0, v[50:51]
	v_lshl_add_u64 v[64:65], v[50:51], 0, v[144:145]
	s_movk_i32 s6, 0x1f5f
	v_cmp_lt_i32_e64 s[6:7], s6, v146
	v_readlane_b32 s69, v248, 10
	v_readlane_b32 s72, v248, 13
	v_readlane_b32 s73, v248, 14
	v_readlane_b32 s74, v248, 15
	v_readlane_b32 s75, v248, 16
	v_readlane_b32 s76, v248, 17
	v_readlane_b32 s77, v248, 18
	v_readlane_b32 s78, v248, 19
	v_readlane_b32 s79, v248, 20
	v_readlane_b32 s80, v248, 21
	v_readlane_b32 s81, v248, 22
	v_readlane_b32 s82, v248, 23
	v_readlane_b32 s83, v248, 24
	s_waitcnt vmcnt(6)
	v_pk_fma_f32 v[48:49], v[48:49], v[58:59], v[54:55]
	v_pk_fma_f32 v[46:47], v[46:47], v[56:57], v[52:53]
	global_store_dwordx4 v[64:65], v[46:49], off
	s_nop 1
	s_waitcnt vmcnt(5)
	v_pk_fma_f32 v[44:45], v[44:45], v[232:233], v[228:229]
	v_pk_fma_f32 v[42:43], v[42:43], v[230:231], v[226:227]
	global_store_dwordx4 v[64:65], v[42:45], off offset:64
	s_nop 1
	s_waitcnt vmcnt(4)
	v_pk_fma_f32 v[40:41], v[40:41], v[240:241], v[236:237]
	v_pk_fma_f32 v[38:39], v[38:39], v[238:239], v[234:235]
	global_store_dwordx4 v[64:65], v[38:41], off offset:512
	s_nop 1
	v_add_u32_e32 v38, 0xa0, v146
	s_waitcnt vmcnt(3)
	v_pk_fma_f32 v[36:37], v[36:37], v[200:201], v[196:197]
	v_pk_fma_f32 v[34:35], v[34:35], v[198:199], v[194:195]
	global_store_dwordx4 v[64:65], v[34:37], off offset:576
	s_and_saveexec_b64 s[26:27], s[6:7]
	s_xor_b64 s[6:7], exec, s[26:27]
	s_cbranch_execz .LBB0_921
	v_add_u32_e32 v134, 0xffffe0a0, v146
	v_readlane_b32 s68, v247, 35
	v_lshlrev_b64 v[34:35], 13, v[134:135]
	v_readlane_b32 s72, v247, 39
	v_readlane_b32 s73, v247, 40
	v_mov_b32_e32 v39, v135
	v_readlane_b32 s69, v247, 36
	v_lshl_add_u64 v[36:37], s[72:73], 0, v[34:35]
	v_lshlrev_b64 v[34:35], 13, v[38:39]
	v_readlane_b32 s70, v247, 37
	v_readlane_b32 s71, v247, 38
	v_readlane_b32 s74, v247, 41
	v_readlane_b32 s75, v247, 42
	v_readlane_b32 s76, v247, 43
	v_readlane_b32 s77, v247, 44
	v_readlane_b32 s78, v247, 45
	v_readlane_b32 s79, v247, 46
	v_readlane_b32 s80, v247, 47
	v_readlane_b32 s81, v247, 48
	v_readlane_b32 s82, v247, 49
	v_readlane_b32 s83, v247, 50

;     __device__ __forceinline__ void operator()(const pg8::f32x4 (&acc)[2][2][4][2], const pg8::Unit& u, int wr, int wc, int fr, int fq) const {
;         const int row0 = u.pm * 256 + wr * 64 + fr, col0 = u.pn * 256 + wc * 32 + 4 * fq;
; #pragma unroll
;         for (int ai = 0; ai < 2; ++ai)
; #pragma unroll
;             for (int m = 0; m < 4; ++m) { const int row = row0 + ai * 128 + m * 16;
;                 const float* rp = (row < NL ? res_lat + (size_t)row * DM : res_ctx + (size_t)(row - NL) * DM) + col0;
;                 const float* gp = gate + rowgrp(row) * MODW + col0;
;                 float* cp = C + (size_t)row * DM + col0;
; #pragma unroll
;                 for (int bj = 0; bj < 2; ++bj)
; #pragma unroll
;                     for (int n = 0; n < 2; ++n) { const pg8::f32x4 r = *(const pg8::f32x4*)(rp + bj * 128 + n * 16), g = *(const pg8::f32x4*)(gp + bj * 128 + n * 16);
;                         *(pg8::f32x4*)(cp + bj * 128 + n * 16) = r + g * acc[ai][bj][m][n]; } }
;     }
.LBB0_923:
	s_or_b64 exec, exec, s[6:7]
	v_lshl_add_u64 v[44:45], v[36:37], 0, v[144:145]
	v_lshrrev_b32_e32 v36, 20, v39
	v_add_u32_e32 v36, v38, v36
	v_ashrrev_i32_e32 v36, 12, v36
	v_mul_i32_i24_e32 v36, 0x3000, v36
	v_cndmask_b32_e32 v36, v158, v36, vcc
	v_ashrrev_i32_e32 v37, 31, v36
	v_lshl_add_u64 v[36:37], v[36:37], 2, s[10:11]
	v_lshl_add_u64 v[46:47], v[36:37], 0, v[144:145]
	global_load_dwordx4 v[36:39], v[44:45], off
	global_load_dwordx4 v[40:43], v[46:47], off
	global_load_dwordx4 v[226:229], v[44:45], off offset:64
	global_load_dwordx4 v[230:233], v[46:47], off offset:64
	global_load_dwordx4 v[234:237], v[44:45], off offset:512
	global_load_dwordx4 v[238:241], v[46:47], off offset:512
	global_load_dwordx4 v[194:197], v[44:45], off offset:576
	global_load_dwordx4 v[198:201], v[46:47], off offset:576
	v_readlane_b32 s68, v248, 9
	v_readlane_b32 s70, v248, 11
	v_readlane_b32 s71, v248, 12
	s_movk_i32 s6, 0x1f50
	v_cmp_gt_i32_e32 vcc, s6, v146
	v_lshl_add_u64 v[34:35], s[70:71], 0, v[34:35]
	v_lshl_add_u64 v[48:49], v[34:35], 0, v[144:145]
	s_movk_i32 s6, 0x1f4f
	v_cmp_lt_i32_e64 s[6:7], s6, v146
	v_readlane_b32 s69, v248, 10
	v_readlane_b32 s72, v248, 13
	v_readlane_b32 s73, v248, 14
	v_readlane_b32 s74, v248, 15
	v_readlane_b32 s75, v248, 16
	v_readlane_b32 s76, v248, 17
	v_readlane_b32 s77, v248, 18
	v_readlane_b32 s78, v248, 19
	v_readlane_b32 s79, v248, 20
	v_readlane_b32 s80, v248, 21
	v_readlane_b32 s81, v248, 22
	v_readlane_b32 s82, v248, 23
	v_readlane_b32 s83, v248, 24
	s_waitcnt vmcnt(6)
	v_pk_fma_f32 v[32:33], v[32:33], v[42:43], v[38:39]
	v_pk_fma_f32 v[30:31], v[30:31], v[40:41], v[36:37]
	global_store_dwordx4 v[48:49], v[30:33], off
	s_nop 1
	s_waitcnt vmcnt(5)
	v_pk_fma_f32 v[28:29], v[28:29], v[232:233], v[228:229]
	v_pk_fma_f32 v[26:27], v[26:27], v[230:231], v[226:227]
	global_store_dwordx4 v[48:49], v[26:29], off offset:64
	s_nop 1
	s_waitcnt vmcnt(4)
	v_pk_fma_f32 v[24:25], v[24:25], v[240:241], v[236:237]
	v_pk_fma_f32 v[22:23], v[22:23], v[238:239], v[234:235]
	global_store_dwordx4 v[48:49], v[22:25], off offset:512
	s_nop 1
	v_add_u32_e32 v22, 0xb0, v146
	s_waitcnt vmcnt(3)
	v_pk_fma_f32 v[20:21], v[20:21], v[200:201], v[196:197]
	v_pk_fma_f32 v[18:19], v[18:19], v[198:199], v[194:195]
	global_store_dwordx4 v[48:49], v[18:21], off offset:576
	s_and_saveexec_b64 s[26:27], s[6:7]
	s_xor_b64 s[6:7], exec, s[26:27]
	s_cbranch_execz .LBB0_925
	v_add_u32_e32 v134, 0xffffe0b0, v146
	v_readlane_b32 s68, v247, 35
	v_lshlrev_b64 v[18:19], 13, v[134:135]
	v_readlane_b32 s72, v247, 39
	v_readlane_b32 s73, v247, 40
	v_mov_b32_e32 v23, v135
	v_readlane_b32 s69, v247, 36
	v_lshl_add_u64 v[20:21], s[72:73], 0, v[18:19]
	v_lshlrev_b64 v[18:19], 13, v[22:23]
	v_readlane_b32 s70, v247, 37
	v_readlane_b32 s71, v247, 38
	v_readlane_b32 s74, v247, 41
	v_readlane_b32 s75, v247, 42
	v_readlane_b32 s76, v247, 43
	v_readlane_b32 s77, v247, 44
	v_readlane_b32 s78, v247, 45
	v_readlane_b32 s79, v247, 46
	v_readlane_b32 s80, v247, 47
	v_readlane_b32 s81, v247, 48
	v_readlane_b32 s82, v247, 49
	v_readlane_b32 s83, v247, 50

; #define PG8_BAR __builtin_amdgcn_s_barrier()
; template <class Epi, class Sched, bool ALIGN_EPI = false, bool SP2 = false>
; __device__ __forceinline__ void gemm_phase(PG8_LAS unsigned char* lds, const Gemm g, const Sched& S, const Epi& E) {
;     ...
;         if constexpr (ALIGN_EPI) { if (wr == 0) PG8_BAR; }
;         if constexpr (!Epi::AFTER_DRAIN) { E(acc, cur, wr, wc, fr, fq); S.done(cur); }
;         if (!has_next) break;
; #pragma unroll
;         for (int a = 0; a < 2; ++a)
; #pragma unroll
;             for (int b = 0; b < 2; ++b)
; #pragma unroll
;                 for (int m = 0; m < 4; ++m)
; #pragma unroll
;                     for (int n = 0; n < 2; ++n) acc[a][b][m][n] = (f32x4){0.f, 0.f, 0.f, 0.f};
;         cur = nxt; cA = nA; cB = nB; ++ui;
;         if constexpr (ALIGN_EPI) { if (wr == 1) PG8_BAR; }
;     }
;     __device__ __forceinline__ void operator()(const pg8::f32x4 (&acc)[2][2][4][2], const pg8::Unit& u, int wr, int wc, int fr, int fq) const {
;         const int row0 = u.pm * 256 + wr * 64 + fr, col0 = u.pn * 256 + wc * 32 + 4 * fq;
; #pragma unroll
;         for (int ai = 0; ai < 2; ++ai)
; #pragma unroll
;             for (int m = 0; m < 4; ++m) { const int row = row0 + ai * 128 + m * 16;
;                 const float* rp = (row < NL ? res_lat + (size_t)row * DM : res_ctx + (size_t)(row - NL) * DM) + col0;
;                 const float* gp = gate + rowgrp(row) * MODW + col0;
;                 float* cp = C + (size_t)row * DM + col0;
; #pragma unroll
;                 for (int bj = 0; bj < 2; ++bj)
; #pragma unroll
;                     for (int n = 0; n < 2; ++n) { const pg8::f32x4 r = *(const pg8::f32x4*)(rp + bj * 128 + n * 16), g = *(const pg8::f32x4*)(gp + bj * 128 + n * 16);
;                         *(pg8::f32x4*)(cp + bj * 128 + n * 16) = r + g * acc[ai][bj][m][n]; } }
;     }
.LBB0_927:
	s_or_b64 exec, exec, s[6:7]
	v_lshl_add_u64 v[26:27], v[20:21], 0, v[144:145]
	v_lshrrev_b32_e32 v20, 20, v23
	v_add_u32_e32 v20, v22, v20
	v_ashrrev_i32_e32 v20, 12, v20
	v_mul_i32_i24_e32 v20, 0x3000, v20
	v_cndmask_b32_e32 v20, v158, v20, vcc
	v_readlane_b32 s68, v248, 9
	v_ashrrev_i32_e32 v21, 31, v20
	v_readlane_b32 s70, v248, 11
	v_readlane_b32 s71, v248, 12
	v_lshl_add_u64 v[20:21], v[20:21], 2, s[10:11]
	v_lshl_add_u64 v[28:29], v[20:21], 0, v[144:145]
	v_lshl_add_u64 v[18:19], s[70:71], 0, v[18:19]
	v_lshl_add_u64 v[30:31], v[18:19], 0, v[144:145]
	global_load_dwordx4 v[18:21], v[26:27], off
	global_load_dwordx4 v[22:25], v[28:29], off
	global_load_dwordx4 v[226:229], v[26:27], off offset:64
	global_load_dwordx4 v[230:233], v[28:29], off offset:64
	global_load_dwordx4 v[234:237], v[26:27], off offset:512
	global_load_dwordx4 v[238:241], v[28:29], off offset:512
	global_load_dwordx4 v[194:197], v[26:27], off offset:576
	global_load_dwordx4 v[198:201], v[28:29], off offset:576
	s_mov_b64 s[6:7], -1
	s_andn2_b64 vcc, exec, s[0:1]
	v_readlane_b32 s69, v248, 10
	v_readlane_b32 s72, v248, 13
	v_readlane_b32 s73, v248, 14
	v_readlane_b32 s74, v248, 15
	v_readlane_b32 s75, v248, 16
	v_readlane_b32 s76, v248, 17
	v_readlane_b32 s77, v248, 18
	v_readlane_b32 s78, v248, 19
	v_readlane_b32 s79, v248, 20
	v_readlane_b32 s80, v248, 21
	v_readlane_b32 s81, v248, 22
	v_readlane_b32 s82, v248, 23
	v_readlane_b32 s83, v248, 24
	s_waitcnt vmcnt(6)
	v_pk_fma_f32 v[16:17], v[16:17], v[24:25], v[20:21]
	v_pk_fma_f32 v[14:15], v[14:15], v[22:23], v[18:19]
	global_store_dwordx4 v[30:31], v[14:17], off
	s_nop 1
	s_waitcnt vmcnt(5)
	v_pk_fma_f32 v[12:13], v[12:13], v[232:233], v[228:229]
	v_pk_fma_f32 v[10:11], v[10:11], v[230:231], v[226:227]
	global_store_dwordx4 v[30:31], v[10:13], off offset:64
	s_nop 1
	s_waitcnt vmcnt(4)
	v_pk_fma_f32 v[8:9], v[8:9], v[240:241], v[236:237]
	v_pk_fma_f32 v[6:7], v[6:7], v[238:239], v[234:235]
	global_store_dwordx4 v[30:31], v[6:9], off offset:512
	s_nop 1
	s_waitcnt vmcnt(3)
	v_pk_fma_f32 v[4:5], v[4:5], v[200:201], v[196:197]
	v_pk_fma_f32 v[2:3], v[2:3], v[198:199], v[194:195]
	global_store_dwordx4 v[30:31], v[2:5], off offset:576
	s_cbranch_vccnz .LBB0_884
	s_andn2_b64 vcc, exec, s[8:9]
	s_cbranch_vccnz .LBB0_883
	s_barrier
	s_branch .LBB0_883

;     __device__ __forceinline__ void operator()(const pg8::f32x4 (&acc)[2][2][4][2], const pg8::Unit& u, int wr, int wc, int fr, int fq) const {
;         const int row0 = u.pm * 256 + wr * 64 + fr, col0 = u.pn * 256 + wc * 32 + 4 * fq;
; #pragma unroll
;         for (int ai = 0; ai < 2; ++ai)
; #pragma unroll
;             for (int m = 0; m < 4; ++m) { const int row = row0 + ai * 128 + m * 16;
;                 const float* rp = (row < NL ? res_lat + (size_t)row * DM : res_ctx + (size_t)(row - NL) * DM) + col0;
;                 const float* gp = gate + rowgrp(row) * MODW + col0;
;                 float* cp = C + (size_t)row * DM + col0;
; #pragma unroll
;                 for (int bj = 0; bj < 2; ++bj)
; #pragma unroll
;                     for (int n = 0; n < 2; ++n) { const pg8::f32x4 r = *(const pg8::f32x4*)(rp + bj * 128 + n * 16), g = *(const pg8::f32x4*)(gp + bj * 128 + n * 16);
;                         *(pg8::f32x4*)(cp + bj * 128 + n * 16) = r + g * acc[ai][bj][m][n]; } }
;     }
.LBB0_1172:
	s_or_b64 exec, exec, s[6:7]
	v_lshrrev_b32_e32 v134, 20, v147
	v_lshl_or_b32 v144, s42, 8, v154
	v_add_u32_e32 v134, v146, v134
	v_ashrrev_i32_e32 v145, 31, v144
	v_ashrrev_i32_e32 v134, 12, v134
	v_lshlrev_b64 v[144:145], 2, v[144:145]
	v_mul_i32_i24_e32 v134, 0x3000, v134
	v_lshl_add_u64 v[160:161], v[150:151], 0, v[144:145]
	v_cndmask_b32_e32 v150, v158, v134, vcc
	v_ashrrev_i32_e32 v151, 31, v150
	v_lshl_add_u64 v[150:151], v[150:151], 2, s[16:17]
	v_lshl_add_u64 v[174:175], v[150:151], 0, v[144:145]
	global_load_dwordx4 v[166:169], v[160:161], off
	global_load_dwordx4 v[170:173], v[174:175], off
	global_load_dwordx4 v[226:229], v[160:161], off offset:64
	global_load_dwordx4 v[230:233], v[174:175], off offset:64
	global_load_dwordx4 v[234:237], v[160:161], off offset:512
	global_load_dwordx4 v[238:241], v[174:175], off offset:512
	global_load_dwordx4 v[194:197], v[160:161], off offset:576
	global_load_dwordx4 v[198:201], v[174:175], off offset:576
	v_readlane_b32 s68, v248, 9
	v_readlane_b32 s72, v248, 13
	v_readlane_b32 s73, v248, 14
	v_readlane_b32 s69, v248, 10
	v_readlane_b32 s70, v248, 11
	v_lshl_add_u64 v[148:149], s[72:73], 0, v[148:149]
	v_lshl_add_u64 v[176:177], v[148:149], 0, v[144:145]
	v_readlane_b32 s71, v248, 12
	v_readlane_b32 s74, v248, 15
	v_readlane_b32 s75, v248, 16
	v_readlane_b32 s76, v248, 17
	v_readlane_b32 s77, v248, 18
	v_readlane_b32 s78, v248, 19
	v_readlane_b32 s79, v248, 20
	v_readlane_b32 s80, v248, 21
	v_readlane_b32 s81, v248, 22
	v_readlane_b32 s82, v248, 23
	v_readlane_b32 s83, v248, 24
	s_waitcnt vmcnt(6)
	v_pk_fma_f32 v[128:129], v[128:129], v[172:173], v[168:169]
	v_pk_fma_f32 v[126:127], v[126:127], v[170:171], v[166:167]
	global_store_dwordx4 v[176:177], v[126:129], off
	s_nop 1
	s_waitcnt vmcnt(5)
	v_pk_fma_f32 v[124:125], v[124:125], v[232:233], v[228:229]
	v_pk_fma_f32 v[122:123], v[122:123], v[230:231], v[226:227]
	global_store_dwordx4 v[176:177], v[122:125], off offset:64
	s_nop 1
	s_waitcnt vmcnt(4)
	v_pk_fma_f32 v[120:121], v[120:121], v[240:241], v[236:237]
	v_pk_fma_f32 v[118:119], v[118:119], v[238:239], v[234:235]
	global_store_dwordx4 v[176:177], v[118:121], off offset:512
	s_nop 1
	v_or_b32_e32 v118, 16, v146
	v_cmp_gt_i32_e32 vcc, s33, v118
	v_cmp_lt_i32_e64 s[6:7], s39, v118
	s_waitcnt vmcnt(3)
	v_pk_fma_f32 v[116:117], v[116:117], v[200:201], v[196:197]
	v_pk_fma_f32 v[114:115], v[114:115], v[198:199], v[194:195]
	global_store_dwordx4 v[176:177], v[114:117], off offset:576
	s_and_saveexec_b64 s[26:27], s[6:7]
	s_xor_b64 s[6:7], exec, s[26:27]
	v_add_u32_e32 v134, 0xffffe010, v146
	v_lshlrev_b64 v[114:115], 13, v[134:135]
	v_mov_b32_e32 v119, v135
	v_lshl_add_u64 v[116:117], s[12:13], 0, v[114:115]
	v_lshlrev_b64 v[114:115], 13, v[118:119]
	s_or_saveexec_b64 s[6:7], s[6:7]
	v_ashrrev_i32_e32 v119, 31, v118
	s_xor_b64 exec, exec, s[6:7]
	s_cbranch_execz .LBB0_1176
	v_readlane_b32 s68, v248, 9
	v_lshlrev_b64 v[114:115], 13, v[118:119]
	v_readlane_b32 s70, v248, 11
	v_readlane_b32 s71, v248, 12
	v_readlane_b32 s69, v248, 10
	v_readlane_b32 s72, v248, 13
	v_lshl_add_u64 v[116:117], s[70:71], 0, v[114:115]
	v_readlane_b32 s73, v248, 14
	v_readlane_b32 s74, v248, 15
	v_readlane_b32 s75, v248, 16
	v_readlane_b32 s76, v248, 17
	v_readlane_b32 s77, v248, 18
	v_readlane_b32 s78, v248, 19
	v_readlane_b32 s79, v248, 20
	v_readlane_b32 s80, v248, 21
	v_readlane_b32 s81, v248, 22
	v_readlane_b32 s82, v248, 23
	v_readlane_b32 s83, v248, 24
.LBB0_1176:
	s_or_b64 exec, exec, s[6:7]
	v_lshl_add_u64 v[124:125], v[116:117], 0, v[144:145]
	v_lshrrev_b32_e32 v116, 20, v119
	v_add_u32_e32 v116, v118, v116
	v_ashrrev_i32_e32 v116, 12, v116
	v_mul_i32_i24_e32 v116, 0x3000, v116
	v_cndmask_b32_e32 v116, v158, v116, vcc
	v_ashrrev_i32_e32 v117, 31, v116
	v_lshl_add_u64 v[116:117], v[116:117], 2, s[16:17]
	v_lshl_add_u64 v[126:127], v[116:117], 0, v[144:145]
	global_load_dwordx4 v[116:119], v[124:125], off
	global_load_dwordx4 v[120:123], v[126:127], off
	global_load_dwordx4 v[226:229], v[124:125], off offset:64
	global_load_dwordx4 v[230:233], v[126:127], off offset:64
	global_load_dwordx4 v[234:237], v[124:125], off offset:512
	global_load_dwordx4 v[238:241], v[126:127], off offset:512
	global_load_dwordx4 v[194:197], v[124:125], off offset:576
	global_load_dwordx4 v[198:201], v[126:127], off offset:576
	v_readlane_b32 s68, v248, 9
	v_readlane_b32 s72, v248, 13
	v_readlane_b32 s73, v248, 14
	v_readlane_b32 s69, v248, 10
	v_readlane_b32 s70, v248, 11
	v_lshl_add_u64 v[114:115], s[72:73], 0, v[114:115]
	v_lshl_add_u64 v[128:129], v[114:115], 0, v[144:145]
	v_readlane_b32 s71, v248, 12
	v_readlane_b32 s74, v248, 15
	v_readlane_b32 s75, v248, 16
	v_readlane_b32 s76, v248, 17
	v_readlane_b32 s77, v248, 18
	v_readlane_b32 s78, v248, 19
	v_readlane_b32 s79, v248, 20
	v_readlane_b32 s80, v248, 21
	v_readlane_b32 s81, v248, 22
	v_readlane_b32 s82, v248, 23
	v_readlane_b32 s83, v248, 24
	s_waitcnt vmcnt(6)
	v_pk_fma_f32 v[112:113], v[112:113], v[122:123], v[118:119]
	v_pk_fma_f32 v[110:111], v[110:111], v[120:121], v[116:117]
	global_store_dwordx4 v[128:129], v[110:113], off
	s_nop 1
	s_waitcnt vmcnt(5)
	v_pk_fma_f32 v[108:109], v[108:109], v[232:233], v[228:229]
	v_pk_fma_f32 v[106:107], v[106:107], v[230:231], v[226:227]
	global_store_dwordx4 v[128:129], v[106:109], off offset:64
	s_nop 1
	s_waitcnt vmcnt(4)
	v_pk_fma_f32 v[104:105], v[104:105], v[240:241], v[236:237]
	v_pk_fma_f32 v[102:103], v[102:103], v[238:239], v[234:235]
	global_store_dwordx4 v[128:129], v[102:105], off offset:512
	s_nop 1
	v_or_b32_e32 v102, 32, v146
	v_cmp_gt_i32_e32 vcc, s33, v102
	v_cmp_lt_i32_e64 s[6:7], s39, v102
	s_waitcnt vmcnt(3)
	v_pk_fma_f32 v[100:101], v[100:101], v[200:201], v[196:197]
	v_pk_fma_f32 v[98:99], v[98:99], v[198:199], v[194:195]
	global_store_dwordx4 v[128:129], v[98:101], off offset:576
	s_and_saveexec_b64 s[26:27], s[6:7]
	s_xor_b64 s[6:7], exec, s[26:27]
	v_add_u32_e32 v134, 0xffffe020, v146
	v_lshlrev_b64 v[98:99], 13, v[134:135]
	v_mov_b32_e32 v103, v135
	v_lshl_add_u64 v[100:101], s[12:13], 0, v[98:99]
	v_lshlrev_b64 v[98:99], 13, v[102:103]
	s_or_saveexec_b64 s[6:7], s[6:7]
	v_ashrrev_i32_e32 v103, 31, v102
	s_xor_b64 exec, exec, s[6:7]
	s_cbranch_execz .LBB0_1180
	v_readlane_b32 s68, v248, 9
	v_lshlrev_b64 v[98:99], 13, v[102:103]
	v_readlane_b32 s70, v248, 11
	v_readlane_b32 s71, v248, 12
	v_readlane_b32 s69, v248, 10
	v_readlane_b32 s72, v248, 13
	v_lshl_add_u64 v[100:101], s[70:71], 0, v[98:99]
	v_readlane_b32 s73, v248, 14
	v_readlane_b32 s74, v248, 15
	v_readlane_b32 s75, v248, 16
	v_readlane_b32 s76, v248, 17
	v_readlane_b32 s77, v248, 18
	v_readlane_b32 s78, v248, 19
	v_readlane_b32 s79, v248, 20
	v_readlane_b32 s80, v248, 21
	v_readlane_b32 s81, v248, 22
	v_readlane_b32 s82, v248, 23
	v_readlane_b32 s83, v248, 24
;     __device__ __forceinline__ void operator()(const pg8::f32x4 (&acc)[2][2][4][2], const pg8::Unit& u, int wr, int wc, int fr, int fq) const {
;         const int row0 = u.pm * 256 + wr * 64 + fr, col0 = u.pn * 256 + wc * 32 + 4 * fq;
; #pragma unroll
;         for (int ai = 0; ai < 2; ++ai)
; #pragma unroll
;             for (int m = 0; m < 4; ++m) { const int row = row0 + ai * 128 + m * 16;
;                 const float* rp = (row < NL ? res_lat + (size_t)row * DM : res_ctx + (size_t)(row - NL) * DM) + col0;
;                 const float* gp = gate + rowgrp(row) * MODW + col0;
;                 float* cp = C + (size_t)row * DM + col0;
; #pragma unroll
;                 for (int bj = 0; bj < 2; ++bj)
; #pragma unroll
;                     for (int n = 0; n < 2; ++n) { const pg8::f32x4 r = *(const pg8::f32x4*)(rp + bj * 128 + n * 16), g = *(const pg8::f32x4*)(gp + bj * 128 + n * 16);
;                         *(pg8::f32x4*)(cp + bj * 128 + n * 16) = r + g * acc[ai][bj][m][n]; } }
;     }
.LBB0_1180:
	s_or_b64 exec, exec, s[6:7]
	v_lshl_add_u64 v[108:109], v[100:101], 0, v[144:145]
	v_lshrrev_b32_e32 v100, 20, v103
	v_add_u32_e32 v100, v102, v100
	v_ashrrev_i32_e32 v100, 12, v100
	v_mul_i32_i24_e32 v100, 0x3000, v100
	v_cndmask_b32_e32 v100, v158, v100, vcc
	v_ashrrev_i32_e32 v101, 31, v100
	v_lshl_add_u64 v[100:101], v[100:101], 2, s[16:17]
	v_lshl_add_u64 v[110:111], v[100:101], 0, v[144:145]
	global_load_dwordx4 v[100:103], v[108:109], off
	global_load_dwordx4 v[104:107], v[110:111], off
	global_load_dwordx4 v[226:229], v[108:109], off offset:64
	global_load_dwordx4 v[230:233], v[110:111], off offset:64
	global_load_dwordx4 v[234:237], v[108:109], off offset:512
	global_load_dwordx4 v[238:241], v[110:111], off offset:512
	global_load_dwordx4 v[194:197], v[108:109], off offset:576
	global_load_dwordx4 v[198:201], v[110:111], off offset:576
	v_readlane_b32 s68, v248, 9
	v_readlane_b32 s72, v248, 13
	v_readlane_b32 s73, v248, 14
	v_readlane_b32 s69, v248, 10
	v_readlane_b32 s70, v248, 11
	v_lshl_add_u64 v[98:99], s[72:73], 0, v[98:99]
	v_lshl_add_u64 v[112:113], v[98:99], 0, v[144:145]
	v_readlane_b32 s71, v248, 12
	v_readlane_b32 s74, v248, 15
	v_readlane_b32 s75, v248, 16
	v_readlane_b32 s76, v248, 17
	v_readlane_b32 s77, v248, 18
	v_readlane_b32 s78, v248, 19
	v_readlane_b32 s79, v248, 20
	v_readlane_b32 s80, v248, 21
	v_readlane_b32 s81, v248, 22
	v_readlane_b32 s82, v248, 23
	v_readlane_b32 s83, v248, 24
	s_waitcnt vmcnt(6)
	v_pk_fma_f32 v[96:97], v[96:97], v[106:107], v[102:103]
	v_pk_fma_f32 v[94:95], v[94:95], v[104:105], v[100:101]
	global_store_dwordx4 v[112:113], v[94:97], off
	s_nop 1
	s_waitcnt vmcnt(5)
	v_pk_fma_f32 v[92:93], v[92:93], v[232:233], v[228:229]
	v_pk_fma_f32 v[90:91], v[90:91], v[230:231], v[226:227]
	global_store_dwordx4 v[112:113], v[90:93], off offset:64
	s_nop 1
	s_waitcnt vmcnt(4)
	v_pk_fma_f32 v[88:89], v[88:89], v[240:241], v[236:237]
	v_pk_fma_f32 v[86:87], v[86:87], v[238:239], v[234:235]
	global_store_dwordx4 v[112:113], v[86:89], off offset:512
	s_nop 1
	v_or_b32_e32 v86, 48, v146
	v_cmp_gt_i32_e32 vcc, s33, v86
	v_cmp_lt_i32_e64 s[6:7], s39, v86
	s_waitcnt vmcnt(3)
	v_pk_fma_f32 v[84:85], v[84:85], v[200:201], v[196:197]
	v_pk_fma_f32 v[82:83], v[82:83], v[198:199], v[194:195]
	global_store_dwordx4 v[112:113], v[82:85], off offset:576
	s_and_saveexec_b64 s[26:27], s[6:7]
	s_xor_b64 s[6:7], exec, s[26:27]
	v_add_u32_e32 v134, 0xffffe030, v146
	v_lshlrev_b64 v[82:83], 13, v[134:135]
	v_mov_b32_e32 v87, v135
	v_lshl_add_u64 v[84:85], s[12:13], 0, v[82:83]
	v_lshlrev_b64 v[82:83], 13, v[86:87]
	s_or_saveexec_b64 s[6:7], s[6:7]
	v_ashrrev_i32_e32 v87, 31, v86
	s_xor_b64 exec, exec, s[6:7]
	s_cbranch_execz .LBB0_1184
	v_readlane_b32 s68, v248, 9
	v_lshlrev_b64 v[82:83], 13, v[86:87]
	v_readlane_b32 s70, v248, 11
	v_readlane_b32 s71, v248, 12
	v_readlane_b32 s69, v248, 10
	v_readlane_b32 s72, v248, 13
	v_lshl_add_u64 v[84:85], s[70:71], 0, v[82:83]
	v_readlane_b32 s73, v248, 14
	v_readlane_b32 s74, v248, 15
	v_readlane_b32 s75, v248, 16
	v_readlane_b32 s76, v248, 17
	v_readlane_b32 s77, v248, 18
	v_readlane_b32 s78, v248, 19
	v_readlane_b32 s79, v248, 20
	v_readlane_b32 s80, v248, 21
	v_readlane_b32 s81, v248, 22
	v_readlane_b32 s82, v248, 23
	v_readlane_b32 s83, v248, 24
.LBB0_1184:
	s_or_b64 exec, exec, s[6:7]
	v_lshl_add_u64 v[92:93], v[84:85], 0, v[144:145]
	v_lshrrev_b32_e32 v84, 20, v87
	v_add_u32_e32 v84, v86, v84
	v_ashrrev_i32_e32 v84, 12, v84
	v_mul_i32_i24_e32 v84, 0x3000, v84
	v_cndmask_b32_e32 v84, v158, v84, vcc
	v_ashrrev_i32_e32 v85, 31, v84
	v_lshl_add_u64 v[84:85], v[84:85], 2, s[16:17]
	v_lshl_add_u64 v[94:95], v[84:85], 0, v[144:145]
	global_load_dwordx4 v[84:87], v[92:93], off
	global_load_dwordx4 v[88:91], v[94:95], off
	global_load_dwordx4 v[226:229], v[92:93], off offset:64
	global_load_dwordx4 v[230:233], v[94:95], off offset:64
	global_load_dwordx4 v[234:237], v[92:93], off offset:512
	global_load_dwordx4 v[238:241], v[94:95], off offset:512
	global_load_dwordx4 v[194:197], v[92:93], off offset:576
	global_load_dwordx4 v[198:201], v[94:95], off offset:576
	v_readlane_b32 s68, v248, 9
	v_readlane_b32 s72, v248, 13
	v_readlane_b32 s73, v248, 14
	s_movk_i32 s6, 0x1f80
	v_cmp_gt_i32_e32 vcc, s6, v146
	v_lshl_add_u64 v[82:83], s[72:73], 0, v[82:83]
	v_lshl_add_u64 v[96:97], v[82:83], 0, v[144:145]
	s_movk_i32 s6, 0x1f7f
	v_cmp_lt_i32_e64 s[6:7], s6, v146
	v_readlane_b32 s69, v248, 10
	v_readlane_b32 s70, v248, 11
	v_readlane_b32 s71, v248, 12
	v_readlane_b32 s74, v248, 15
	v_readlane_b32 s75, v248, 16
	v_readlane_b32 s76, v248, 17
	v_readlane_b32 s77, v248, 18
	v_readlane_b32 s78, v248, 19
	v_readlane_b32 s79, v248, 20
	v_readlane_b32 s80, v248, 21
	v_readlane_b32 s81, v248, 22
	v_readlane_b32 s82, v248, 23
	v_readlane_b32 s83, v248, 24
	s_waitcnt vmcnt(6)
	v_pk_fma_f32 v[80:81], v[80:81], v[90:91], v[86:87]
	v_pk_fma_f32 v[78:79], v[78:79], v[88:89], v[84:85]
	global_store_dwordx4 v[96:97], v[78:81], off
	s_nop 1
	s_waitcnt vmcnt(5)
	v_pk_fma_f32 v[76:77], v[76:77], v[232:233], v[228:229]
	v_pk_fma_f32 v[74:75], v[74:75], v[230:231], v[226:227]
	global_store_dwordx4 v[96:97], v[74:77], off offset:64
	s_nop 1
	s_waitcnt vmcnt(4)
	v_pk_fma_f32 v[72:73], v[72:73], v[240:241], v[236:237]
	v_pk_fma_f32 v[70:71], v[70:71], v[238:239], v[234:235]
	global_store_dwordx4 v[96:97], v[70:73], off offset:512
	s_nop 1
	v_add_u32_e32 v70, 0x80, v146
	s_waitcnt vmcnt(3)
	v_pk_fma_f32 v[68:69], v[68:69], v[200:201], v[196:197]
	v_pk_fma_f32 v[66:67], v[66:67], v[198:199], v[194:195]
	global_store_dwordx4 v[96:97], v[66:69], off offset:576
	s_and_saveexec_b64 s[26:27], s[6:7]
	s_xor_b64 s[6:7], exec, s[26:27]
	v_add_u32_e32 v134, 0xffffe080, v146
	v_lshlrev_b64 v[66:67], 13, v[134:135]
	v_mov_b32_e32 v71, v135
	v_lshl_add_u64 v[68:69], s[12:13], 0, v[66:67]
	v_lshlrev_b64 v[66:67], 13, v[70:71]
	s_or_saveexec_b64 s[6:7], s[6:7]
	v_ashrrev_i32_e32 v71, 31, v70
	s_xor_b64 exec, exec, s[6:7]
	s_cbranch_execz .LBB0_1188
	v_readlane_b32 s68, v248, 9
	v_lshlrev_b64 v[66:67], 13, v[70:71]
	v_readlane_b32 s70, v248, 11
	v_readlane_b32 s71, v248, 12
	v_readlane_b32 s69, v248, 10
	v_readlane_b32 s72, v248, 13
	v_lshl_add_u64 v[68:69], s[70:71], 0, v[66:67]
	v_readlane_b32 s73, v248, 14
	v_readlane_b32 s74, v248, 15
	v_readlane_b32 s75, v248, 16
	v_readlane_b32 s76, v248, 17
	v_readlane_b32 s77, v248, 18
	v_readlane_b32 s78, v248, 19
	v_readlane_b32 s79, v248, 20
	v_readlane_b32 s80, v248, 21
	v_readlane_b32 s81, v248, 22
	v_readlane_b32 s82, v248, 23
	v_readlane_b32 s83, v248, 24
;     __device__ __forceinline__ void operator()(const pg8::f32x4 (&acc)[2][2][4][2], const pg8::Unit& u, int wr, int wc, int fr, int fq) const {
;         const int row0 = u.pm * 256 + wr * 64 + fr, col0 = u.pn * 256 + wc * 32 + 4 * fq;
; #pragma unroll
;         for (int ai = 0; ai < 2; ++ai)
; #pragma unroll
;             for (int m = 0; m < 4; ++m) { const int row = row0 + ai * 128 + m * 16;
;                 const float* rp = (row < NL ? res_lat + (size_t)row * DM : res_ctx + (size_t)(row - NL) * DM) + col0;
;                 const float* gp = gate + rowgrp(row) * MODW + col0;
;                 float* cp = C + (size_t)row * DM + col0;
; #pragma unroll
;                 for (int bj = 0; bj < 2; ++bj)
; #pragma unroll
;                     for (int n = 0; n < 2; ++n) { const pg8::f32x4 r = *(const pg8::f32x4*)(rp + bj * 128 + n * 16), g = *(const pg8::f32x4*)(gp + bj * 128 + n * 16);
;                         *(pg8::f32x4*)(cp + bj * 128 + n * 16) = r + g * acc[ai][bj][m][n]; } }
;     }
.LBB0_1188:
	s_or_b64 exec, exec, s[6:7]
	v_lshl_add_u64 v[76:77], v[68:69], 0, v[144:145]
	v_lshrrev_b32_e32 v68, 20, v71
	v_add_u32_e32 v68, v70, v68
	v_ashrrev_i32_e32 v68, 12, v68
	v_mul_i32_i24_e32 v68, 0x3000, v68
	v_cndmask_b32_e32 v68, v158, v68, vcc
	v_ashrrev_i32_e32 v69, 31, v68
	v_lshl_add_u64 v[68:69], v[68:69], 2, s[16:17]
	v_lshl_add_u64 v[78:79], v[68:69], 0, v[144:145]
	global_load_dwordx4 v[68:71], v[76:77], off
	global_load_dwordx4 v[72:75], v[78:79], off
	global_load_dwordx4 v[226:229], v[76:77], off offset:64
	global_load_dwordx4 v[230:233], v[78:79], off offset:64
	global_load_dwordx4 v[234:237], v[76:77], off offset:512
	global_load_dwordx4 v[238:241], v[78:79], off offset:512
	global_load_dwordx4 v[194:197], v[76:77], off offset:576
	global_load_dwordx4 v[198:201], v[78:79], off offset:576
	v_readlane_b32 s68, v248, 9
	v_readlane_b32 s72, v248, 13
	v_readlane_b32 s73, v248, 14
	s_movk_i32 s6, 0x1f70
	v_cmp_gt_i32_e32 vcc, s6, v146
	v_lshl_add_u64 v[66:67], s[72:73], 0, v[66:67]
	v_lshl_add_u64 v[80:81], v[66:67], 0, v[144:145]
	s_movk_i32 s6, 0x1f6f
	v_cmp_lt_i32_e64 s[6:7], s6, v146
	v_readlane_b32 s69, v248, 10
	v_readlane_b32 s70, v248, 11
	v_readlane_b32 s71, v248, 12
	v_readlane_b32 s74, v248, 15
	v_readlane_b32 s75, v248, 16
	v_readlane_b32 s76, v248, 17
	v_readlane_b32 s77, v248, 18
	v_readlane_b32 s78, v248, 19
	v_readlane_b32 s79, v248, 20
	v_readlane_b32 s80, v248, 21
	v_readlane_b32 s81, v248, 22
	v_readlane_b32 s82, v248, 23
	v_readlane_b32 s83, v248, 24
	s_waitcnt vmcnt(6)
	v_pk_fma_f32 v[64:65], v[64:65], v[74:75], v[70:71]
	v_pk_fma_f32 v[62:63], v[62:63], v[72:73], v[68:69]
	global_store_dwordx4 v[80:81], v[62:65], off
	s_nop 1
	s_waitcnt vmcnt(5)
	v_pk_fma_f32 v[60:61], v[60:61], v[232:233], v[228:229]
	v_pk_fma_f32 v[58:59], v[58:59], v[230:231], v[226:227]
	global_store_dwordx4 v[80:81], v[58:61], off offset:64
	s_nop 1
	s_waitcnt vmcnt(4)
	v_pk_fma_f32 v[56:57], v[56:57], v[240:241], v[236:237]
	v_pk_fma_f32 v[54:55], v[54:55], v[238:239], v[234:235]
	global_store_dwordx4 v[80:81], v[54:57], off offset:512
	s_nop 1
	v_add_u32_e32 v54, 0x90, v146
	s_waitcnt vmcnt(3)
	v_pk_fma_f32 v[52:53], v[52:53], v[200:201], v[196:197]
	v_pk_fma_f32 v[50:51], v[50:51], v[198:199], v[194:195]
	global_store_dwordx4 v[80:81], v[50:53], off offset:576
	s_and_saveexec_b64 s[26:27], s[6:7]
	s_xor_b64 s[6:7], exec, s[26:27]
	v_add_u32_e32 v134, 0xffffe090, v146
	v_lshlrev_b64 v[50:51], 13, v[134:135]
	v_mov_b32_e32 v55, v135
	v_lshl_add_u64 v[52:53], s[12:13], 0, v[50:51]
	v_lshlrev_b64 v[50:51], 13, v[54:55]
	s_or_saveexec_b64 s[6:7], s[6:7]
	v_ashrrev_i32_e32 v55, 31, v54
	s_xor_b64 exec, exec, s[6:7]
	s_cbranch_execz .LBB0_1192
	v_readlane_b32 s68, v248, 9
	v_lshlrev_b64 v[50:51], 13, v[54:55]
	v_readlane_b32 s70, v248, 11
	v_readlane_b32 s71, v248, 12
	v_readlane_b32 s69, v248, 10
	v_readlane_b32 s72, v248, 13
	v_lshl_add_u64 v[52:53], s[70:71], 0, v[50:51]
	v_readlane_b32 s73, v248, 14
	v_readlane_b32 s74, v248, 15
	v_readlane_b32 s75, v248, 16
	v_readlane_b32 s76, v248, 17
	v_readlane_b32 s77, v248, 18
	v_readlane_b32 s78, v248, 19
	v_readlane_b32 s79, v248, 20
	v_readlane_b32 s80, v248, 21
	v_readlane_b32 s81, v248, 22
	v_readlane_b32 s82, v248, 23
	v_readlane_b32 s83, v248, 24
.LBB0_1192:
	s_or_b64 exec, exec, s[6:7]
	v_lshl_add_u64 v[60:61], v[52:53], 0, v[144:145]
	v_lshrrev_b32_e32 v52, 20, v55
	v_add_u32_e32 v52, v54, v52
	v_ashrrev_i32_e32 v52, 12, v52
	v_mul_i32_i24_e32 v52, 0x3000, v52
	v_cndmask_b32_e32 v52, v158, v52, vcc
	v_ashrrev_i32_e32 v53, 31, v52
	v_lshl_add_u64 v[52:53], v[52:53], 2, s[16:17]
	v_lshl_add_u64 v[62:63], v[52:53], 0, v[144:145]
	global_load_dwordx4 v[52:55], v[60:61], off
	global_load_dwordx4 v[56:59], v[62:63], off
	global_load_dwordx4 v[226:229], v[60:61], off offset:64
	global_load_dwordx4 v[230:233], v[62:63], off offset:64
	global_load_dwordx4 v[234:237], v[60:61], off offset:512
	global_load_dwordx4 v[238:241], v[62:63], off offset:512
	global_load_dwordx4 v[194:197], v[60:61], off offset:576
	global_load_dwordx4 v[198:201], v[62:63], off offset:576
	v_readlane_b32 s68, v248, 9
	v_readlane_b32 s72, v248, 13
	v_readlane_b32 s73, v248, 14
	s_movk_i32 s6, 0x1f60
	v_cmp_gt_i32_e32 vcc, s6, v146
	v_lshl_add_u64 v[50:51], s[72:73], 0, v[50:51]
	v_lshl_add_u64 v[64:65], v[50:51], 0, v[144:145]
	s_movk_i32 s6, 0x1f5f
	v_cmp_lt_i32_e64 s[6:7], s6, v146
	v_readlane_b32 s69, v248, 10
	v_readlane_b32 s70, v248, 11
	v_readlane_b32 s71, v248, 12
	v_readlane_b32 s74, v248, 15
	v_readlane_b32 s75, v248, 16
	v_readlane_b32 s76, v248, 17
	v_readlane_b32 s77, v248, 18
	v_readlane_b32 s78, v248, 19
	v_readlane_b32 s79, v248, 20
	v_readlane_b32 s80, v248, 21
	v_readlane_b32 s81, v248, 22
	v_readlane_b32 s82, v248, 23
	v_readlane_b32 s83, v248, 24
	s_waitcnt vmcnt(6)
	v_pk_fma_f32 v[48:49], v[48:49], v[58:59], v[54:55]
	v_pk_fma_f32 v[46:47], v[46:47], v[56:57], v[52:53]
	global_store_dwordx4 v[64:65], v[46:49], off
	s_nop 1
	s_waitcnt vmcnt(5)
	v_pk_fma_f32 v[44:45], v[44:45], v[232:233], v[228:229]
	v_pk_fma_f32 v[42:43], v[42:43], v[230:231], v[226:227]
	global_store_dwordx4 v[64:65], v[42:45], off offset:64
	s_nop 1
	s_waitcnt vmcnt(4)
	v_pk_fma_f32 v[40:41], v[40:41], v[240:241], v[236:237]
	v_pk_fma_f32 v[38:39], v[38:39], v[238:239], v[234:235]
	global_store_dwordx4 v[64:65], v[38:41], off offset:512
	s_nop 1
	v_add_u32_e32 v38, 0xa0, v146
	s_waitcnt vmcnt(3)
	v_pk_fma_f32 v[36:37], v[36:37], v[200:201], v[196:197]
	v_pk_fma_f32 v[34:35], v[34:35], v[198:199], v[194:195]
	global_store_dwordx4 v[64:65], v[34:37], off offset:576
	s_and_saveexec_b64 s[26:27], s[6:7]
	s_xor_b64 s[6:7], exec, s[26:27]
	v_add_u32_e32 v134, 0xffffe0a0, v146
	v_lshlrev_b64 v[34:35], 13, v[134:135]
	v_mov_b32_e32 v39, v135
	v_lshl_add_u64 v[36:37], s[12:13], 0, v[34:35]
	v_lshlrev_b64 v[34:35], 13, v[38:39]
	s_or_saveexec_b64 s[6:7], s[6:7]
	v_ashrrev_i32_e32 v39, 31, v38
	s_xor_b64 exec, exec, s[6:7]
	s_cbranch_execz .LBB0_1196
	v_readlane_b32 s68, v248, 9
	v_lshlrev_b64 v[34:35], 13, v[38:39]
	v_readlane_b32 s70, v248, 11
	v_readlane_b32 s71, v248, 12
	v_readlane_b32 s69, v248, 10
	v_readlane_b32 s72, v248, 13
	v_lshl_add_u64 v[36:37], s[70:71], 0, v[34:35]
	v_readlane_b32 s73, v248, 14
	v_readlane_b32 s74, v248, 15
	v_readlane_b32 s75, v248, 16
	v_readlane_b32 s76, v248, 17
	v_readlane_b32 s77, v248, 18
	v_readlane_b32 s78, v248, 19
	v_readlane_b32 s79, v248, 20
	v_readlane_b32 s80, v248, 21
	v_readlane_b32 s81, v248, 22
	v_readlane_b32 s82, v248, 23
	v_readlane_b32 s83, v248, 24
;     __device__ __forceinline__ void operator()(const pg8::f32x4 (&acc)[2][2][4][2], const pg8::Unit& u, int wr, int wc, int fr, int fq) const {
;         const int row0 = u.pm * 256 + wr * 64 + fr, col0 = u.pn * 256 + wc * 32 + 4 * fq;
; #pragma unroll
;         for (int ai = 0; ai < 2; ++ai)
; #pragma unroll
;             for (int m = 0; m < 4; ++m) { const int row = row0 + ai * 128 + m * 16;
;                 const float* rp = (row < NL ? res_lat + (size_t)row * DM : res_ctx + (size_t)(row - NL) * DM) + col0;
;                 const float* gp = gate + rowgrp(row) * MODW + col0;
;                 float* cp = C + (size_t)row * DM + col0;
; #pragma unroll
;                 for (int bj = 0; bj < 2; ++bj)
; #pragma unroll
;                     for (int n = 0; n < 2; ++n) { const pg8::f32x4 r = *(const pg8::f32x4*)(rp + bj * 128 + n * 16), g = *(const pg8::f32x4*)(gp + bj * 128 + n * 16);
;                         *(pg8::f32x4*)(cp + bj * 128 + n * 16) = r + g * acc[ai][bj][m][n]; } }
;     }
.LBB0_1196:
	s_or_b64 exec, exec, s[6:7]
	v_lshl_add_u64 v[44:45], v[36:37], 0, v[144:145]
	v_lshrrev_b32_e32 v36, 20, v39
	v_add_u32_e32 v36, v38, v36
	v_ashrrev_i32_e32 v36, 12, v36
	v_mul_i32_i24_e32 v36, 0x3000, v36
	v_cndmask_b32_e32 v36, v158, v36, vcc
	v_ashrrev_i32_e32 v37, 31, v36
	v_lshl_add_u64 v[36:37], v[36:37], 2, s[16:17]
	v_lshl_add_u64 v[46:47], v[36:37], 0, v[144:145]
	global_load_dwordx4 v[36:39], v[44:45], off
	global_load_dwordx4 v[40:43], v[46:47], off
	global_load_dwordx4 v[226:229], v[44:45], off offset:64
	global_load_dwordx4 v[230:233], v[46:47], off offset:64
	global_load_dwordx4 v[234:237], v[44:45], off offset:512
	global_load_dwordx4 v[238:241], v[46:47], off offset:512
	global_load_dwordx4 v[194:197], v[44:45], off offset:576
	global_load_dwordx4 v[198:201], v[46:47], off offset:576
	v_readlane_b32 s68, v248, 9
	v_readlane_b32 s72, v248, 13
	v_readlane_b32 s73, v248, 14
	s_movk_i32 s6, 0x1f50
	v_cmp_gt_i32_e32 vcc, s6, v146
	v_lshl_add_u64 v[34:35], s[72:73], 0, v[34:35]
	v_lshl_add_u64 v[48:49], v[34:35], 0, v[144:145]
	s_movk_i32 s6, 0x1f4f
	v_cmp_lt_i32_e64 s[6:7], s6, v146
	v_readlane_b32 s69, v248, 10
	v_readlane_b32 s70, v248, 11
	v_readlane_b32 s71, v248, 12
	v_readlane_b32 s74, v248, 15
	v_readlane_b32 s75, v248, 16
	v_readlane_b32 s76, v248, 17
	v_readlane_b32 s77, v248, 18
	v_readlane_b32 s78, v248, 19
	v_readlane_b32 s79, v248, 20
	v_readlane_b32 s80, v248, 21
	v_readlane_b32 s81, v248, 22
	v_readlane_b32 s82, v248, 23
	v_readlane_b32 s83, v248, 24
	s_waitcnt vmcnt(6)
	v_pk_fma_f32 v[32:33], v[32:33], v[42:43], v[38:39]
	v_pk_fma_f32 v[30:31], v[30:31], v[40:41], v[36:37]
	global_store_dwordx4 v[48:49], v[30:33], off
	s_nop 1
	s_waitcnt vmcnt(5)
	v_pk_fma_f32 v[28:29], v[28:29], v[232:233], v[228:229]
	v_pk_fma_f32 v[26:27], v[26:27], v[230:231], v[226:227]
	global_store_dwordx4 v[48:49], v[26:29], off offset:64
	s_nop 1
	s_waitcnt vmcnt(4)
	v_pk_fma_f32 v[24:25], v[24:25], v[240:241], v[236:237]
	v_pk_fma_f32 v[22:23], v[22:23], v[238:239], v[234:235]
	global_store_dwordx4 v[48:49], v[22:25], off offset:512
	s_nop 1
	v_add_u32_e32 v22, 0xb0, v146
	s_waitcnt vmcnt(3)
	v_pk_fma_f32 v[20:21], v[20:21], v[200:201], v[196:197]
	v_pk_fma_f32 v[18:19], v[18:19], v[198:199], v[194:195]
	global_store_dwordx4 v[48:49], v[18:21], off offset:576
	s_and_saveexec_b64 s[26:27], s[6:7]
	s_xor_b64 s[6:7], exec, s[26:27]
	v_add_u32_e32 v134, 0xffffe0b0, v146
	v_lshlrev_b64 v[18:19], 13, v[134:135]
	v_mov_b32_e32 v23, v135
	v_lshl_add_u64 v[20:21], s[12:13], 0, v[18:19]
	v_lshlrev_b64 v[18:19], 13, v[22:23]
	s_or_saveexec_b64 s[6:7], s[6:7]
	v_ashrrev_i32_e32 v23, 31, v22
	s_xor_b64 exec, exec, s[6:7]
	s_cbranch_execz .LBB0_1200
	v_readlane_b32 s68, v248, 9
	v_lshlrev_b64 v[18:19], 13, v[22:23]
	v_readlane_b32 s70, v248, 11
	v_readlane_b32 s71, v248, 12
	v_readlane_b32 s69, v248, 10
	v_readlane_b32 s72, v248, 13
	v_lshl_add_u64 v[20:21], s[70:71], 0, v[18:19]
	v_readlane_b32 s73, v248, 14
	v_readlane_b32 s74, v248, 15
	v_readlane_b32 s75, v248, 16
	v_readlane_b32 s76, v248, 17
	v_readlane_b32 s77, v248, 18
	v_readlane_b32 s78, v248, 19
	v_readlane_b32 s79, v248, 20
	v_readlane_b32 s80, v248, 21
	v_readlane_b32 s81, v248, 22
	v_readlane_b32 s82, v248, 23
	v_readlane_b32 s83, v248, 24
.LBB0_1200:
	s_or_b64 exec, exec, s[6:7]
	v_lshl_add_u64 v[26:27], v[20:21], 0, v[144:145]
	v_lshrrev_b32_e32 v20, 20, v23
	v_add_u32_e32 v20, v22, v20
	v_ashrrev_i32_e32 v20, 12, v20
	v_mul_i32_i24_e32 v20, 0x3000, v20
	v_cndmask_b32_e32 v20, v158, v20, vcc
	v_readlane_b32 s68, v248, 9
	v_ashrrev_i32_e32 v21, 31, v20
	v_readlane_b32 s72, v248, 13
	v_readlane_b32 s73, v248, 14
	v_lshl_add_u64 v[20:21], v[20:21], 2, s[16:17]
	v_lshl_add_u64 v[28:29], v[20:21], 0, v[144:145]
	v_lshl_add_u64 v[18:19], s[72:73], 0, v[18:19]
	v_lshl_add_u64 v[30:31], v[18:19], 0, v[144:145]
	global_load_dwordx4 v[18:21], v[26:27], off
	global_load_dwordx4 v[22:25], v[28:29], off
	global_load_dwordx4 v[226:229], v[26:27], off offset:64
	global_load_dwordx4 v[230:233], v[28:29], off offset:64
	global_load_dwordx4 v[234:237], v[26:27], off offset:512
	global_load_dwordx4 v[238:241], v[28:29], off offset:512
	global_load_dwordx4 v[194:197], v[26:27], off offset:576
	global_load_dwordx4 v[198:201], v[28:29], off offset:576
	s_mov_b64 s[6:7], -1
	s_and_b64 vcc, exec, s[0:1]
	v_readlane_b32 s69, v248, 10
	v_readlane_b32 s70, v248, 11
	v_readlane_b32 s71, v248, 12
	v_readlane_b32 s74, v248, 15
	v_readlane_b32 s75, v248, 16
	v_readlane_b32 s76, v248, 17
	v_readlane_b32 s77, v248, 18
	v_readlane_b32 s78, v248, 19
	v_readlane_b32 s79, v248, 20
	v_readlane_b32 s80, v248, 21
	v_readlane_b32 s81, v248, 22
	v_readlane_b32 s82, v248, 23
	v_readlane_b32 s83, v248, 24
	s_waitcnt vmcnt(6)
	v_pk_fma_f32 v[16:17], v[16:17], v[24:25], v[20:21]
	v_pk_fma_f32 v[14:15], v[14:15], v[22:23], v[18:19]
	global_store_dwordx4 v[30:31], v[14:17], off
	s_nop 1
	s_waitcnt vmcnt(5)
	v_pk_fma_f32 v[12:13], v[12:13], v[232:233], v[228:229]
	v_pk_fma_f32 v[10:11], v[10:11], v[230:231], v[226:227]
	global_store_dwordx4 v[30:31], v[10:13], off offset:64
	s_nop 1
	s_waitcnt vmcnt(4)
	v_pk_fma_f32 v[8:9], v[8:9], v[240:241], v[236:237]
	v_pk_fma_f32 v[6:7], v[6:7], v[238:239], v[234:235]
	global_store_dwordx4 v[30:31], v[6:9], off offset:512
	s_nop 1
	s_waitcnt vmcnt(3)
	v_pk_fma_f32 v[4:5], v[4:5], v[200:201], v[196:197]
	v_pk_fma_f32 v[2:3], v[2:3], v[198:199], v[194:195]
	global_store_dwordx4 v[30:31], v[2:5], off offset:576
	s_cbranch_vccnz .LBB0_1153
	s_andn2_b64 vcc, exec, s[14:15]
	s_cbranch_vccnz .LBB0_1152
	s_barrier
	s_branch .LBB0_1152

;     __device__ __forceinline__ void operator()(const pg8::f32x4 (&acc)[2][2][4][2], const pg8::Unit& u, int wr, int wc, int fr, int fq) const {
;         const int row0 = u.pm * 256 + wr * 64 + fr, col0 = u.pn * 256 + wc * 32 + 4 * fq;
; #pragma unroll
;         for (int ai = 0; ai < 2; ++ai)
; #pragma unroll
;             for (int m = 0; m < 4; ++m) { const int row = row0 + ai * 128 + m * 16;
;                 const float* rp = (row < NL ? res_lat + (size_t)row * DM : res_ctx + (size_t)(row - NL) * DM) + col0;
;                 const float* gp = gate + rowgrp(row) * MODW + col0;
;                 float* cp = C + (size_t)row * DM + col0;
; #pragma unroll
;                 for (int bj = 0; bj < 2; ++bj)
; #pragma unroll
;                     for (int n = 0; n < 2; ++n) { const pg8::f32x4 r = *(const pg8::f32x4*)(rp + bj * 128 + n * 16), g = *(const pg8::f32x4*)(gp + bj * 128 + n * 16);
;                         *(pg8::f32x4*)(cp + bj * 128 + n * 16) = r + g * acc[ai][bj][m][n]; } }
;     }
.LBB0_1835:
	s_or_b64 exec, exec, s[4:5]
	v_lshrrev_b32_e32 v134, 20, v147
	v_lshl_or_b32 v144, s24, 8, v154
	v_add_u32_e32 v134, v146, v134
	v_ashrrev_i32_e32 v145, 31, v144
	v_ashrrev_i32_e32 v134, 12, v134
	v_lshlrev_b64 v[144:145], 2, v[144:145]
	v_mul_i32_i24_e32 v134, 0x3000, v134
	v_lshl_add_u64 v[160:161], v[150:151], 0, v[144:145]
	v_cndmask_b32_e32 v150, v158, v134, vcc
	v_ashrrev_i32_e32 v151, 31, v150
	v_lshl_add_u64 v[150:151], v[150:151], 2, s[10:11]
	v_lshl_add_u64 v[174:175], v[150:151], 0, v[144:145]
	global_load_dwordx4 v[166:169], v[160:161], off
	global_load_dwordx4 v[170:173], v[174:175], off
	global_load_dwordx4 v[226:229], v[160:161], off offset:64
	global_load_dwordx4 v[230:233], v[174:175], off offset:64
	global_load_dwordx4 v[234:237], v[160:161], off offset:512
	global_load_dwordx4 v[238:241], v[174:175], off offset:512
	global_load_dwordx4 v[194:197], v[160:161], off offset:576
	global_load_dwordx4 v[198:201], v[174:175], off offset:576
	v_readlane_b32 s68, v248, 9
	v_readlane_b32 s70, v248, 11
	v_readlane_b32 s71, v248, 12
	v_readlane_b32 s69, v248, 10
	v_readlane_b32 s72, v248, 13
	v_lshl_add_u64 v[148:149], s[70:71], 0, v[148:149]
	v_lshl_add_u64 v[176:177], v[148:149], 0, v[144:145]
	v_readlane_b32 s73, v248, 14
	v_readlane_b32 s74, v248, 15
	v_readlane_b32 s75, v248, 16
	v_readlane_b32 s76, v248, 17
	v_readlane_b32 s77, v248, 18
	v_readlane_b32 s78, v248, 19
	v_readlane_b32 s79, v248, 20
	v_readlane_b32 s80, v248, 21
	v_readlane_b32 s81, v248, 22
	v_readlane_b32 s82, v248, 23
	v_readlane_b32 s83, v248, 24
	s_waitcnt vmcnt(6)
	v_pk_fma_f32 v[128:129], v[128:129], v[172:173], v[168:169]
	v_pk_fma_f32 v[126:127], v[126:127], v[170:171], v[166:167]
	global_store_dwordx4 v[176:177], v[126:129], off
	s_nop 1
	s_waitcnt vmcnt(5)
	v_pk_fma_f32 v[124:125], v[124:125], v[232:233], v[228:229]
	v_pk_fma_f32 v[122:123], v[122:123], v[230:231], v[226:227]
	global_store_dwordx4 v[176:177], v[122:125], off offset:64
	s_nop 1
	s_waitcnt vmcnt(4)
	v_pk_fma_f32 v[120:121], v[120:121], v[240:241], v[236:237]
	v_pk_fma_f32 v[118:119], v[118:119], v[238:239], v[234:235]
	global_store_dwordx4 v[176:177], v[118:121], off offset:512
	s_nop 1
	v_or_b32_e32 v118, 16, v146
	v_cmp_gt_i32_e32 vcc, s36, v118
	v_cmp_lt_i32_e64 s[4:5], s42, v118
	s_waitcnt vmcnt(3)
	v_pk_fma_f32 v[116:117], v[116:117], v[200:201], v[196:197]
	v_pk_fma_f32 v[114:115], v[114:115], v[198:199], v[194:195]
	global_store_dwordx4 v[176:177], v[114:117], off offset:576
	s_and_saveexec_b64 s[28:29], s[4:5]
	s_xor_b64 s[4:5], exec, s[28:29]
	v_add_u32_e32 v134, 0xffffe010, v146
	v_lshlrev_b64 v[114:115], 13, v[134:135]
	v_mov_b32_e32 v119, v135
	v_lshl_add_u64 v[116:117], s[8:9], 0, v[114:115]
	v_lshlrev_b64 v[114:115], 13, v[118:119]
	s_or_saveexec_b64 s[4:5], s[4:5]
	v_ashrrev_i32_e32 v119, 31, v118
	s_xor_b64 exec, exec, s[4:5]
	s_cbranch_execz .LBB0_1839
	v_readlane_b32 s68, v248, 9
	v_lshlrev_b64 v[114:115], 13, v[118:119]
	v_readlane_b32 s72, v248, 13
	v_readlane_b32 s73, v248, 14
	v_readlane_b32 s69, v248, 10
	v_readlane_b32 s70, v248, 11
	v_lshl_add_u64 v[116:117], s[72:73], 0, v[114:115]
	v_readlane_b32 s71, v248, 12
	v_readlane_b32 s74, v248, 15
	v_readlane_b32 s75, v248, 16
	v_readlane_b32 s76, v248, 17
	v_readlane_b32 s77, v248, 18
	v_readlane_b32 s78, v248, 19
	v_readlane_b32 s79, v248, 20
	v_readlane_b32 s80, v248, 21
	v_readlane_b32 s81, v248, 22
	v_readlane_b32 s82, v248, 23
	v_readlane_b32 s83, v248, 24
.LBB0_1839:
	s_or_b64 exec, exec, s[4:5]
	v_lshl_add_u64 v[124:125], v[116:117], 0, v[144:145]
	v_lshrrev_b32_e32 v116, 20, v119
	v_add_u32_e32 v116, v118, v116
	v_ashrrev_i32_e32 v116, 12, v116
	v_mul_i32_i24_e32 v116, 0x3000, v116
	v_cndmask_b32_e32 v116, v158, v116, vcc
	v_ashrrev_i32_e32 v117, 31, v116
	v_lshl_add_u64 v[116:117], v[116:117], 2, s[10:11]
	v_lshl_add_u64 v[126:127], v[116:117], 0, v[144:145]
	global_load_dwordx4 v[116:119], v[124:125], off
	global_load_dwordx4 v[120:123], v[126:127], off
	global_load_dwordx4 v[226:229], v[124:125], off offset:64
	global_load_dwordx4 v[230:233], v[126:127], off offset:64
	global_load_dwordx4 v[234:237], v[124:125], off offset:512
	global_load_dwordx4 v[238:241], v[126:127], off offset:512
	global_load_dwordx4 v[194:197], v[124:125], off offset:576
	global_load_dwordx4 v[198:201], v[126:127], off offset:576
	v_readlane_b32 s68, v248, 9
	v_readlane_b32 s70, v248, 11
	v_readlane_b32 s71, v248, 12
	v_readlane_b32 s69, v248, 10
	v_readlane_b32 s72, v248, 13
	v_lshl_add_u64 v[114:115], s[70:71], 0, v[114:115]
	v_lshl_add_u64 v[128:129], v[114:115], 0, v[144:145]
	v_readlane_b32 s73, v248, 14
	v_readlane_b32 s74, v248, 15
	v_readlane_b32 s75, v248, 16
	v_readlane_b32 s76, v248, 17
	v_readlane_b32 s77, v248, 18
	v_readlane_b32 s78, v248, 19
	v_readlane_b32 s79, v248, 20
	v_readlane_b32 s80, v248, 21
	v_readlane_b32 s81, v248, 22
	v_readlane_b32 s82, v248, 23
	v_readlane_b32 s83, v248, 24
	s_waitcnt vmcnt(6)
	v_pk_fma_f32 v[112:113], v[112:113], v[122:123], v[118:119]
	v_pk_fma_f32 v[110:111], v[110:111], v[120:121], v[116:117]
	global_store_dwordx4 v[128:129], v[110:113], off
	s_nop 1
	s_waitcnt vmcnt(5)
	v_pk_fma_f32 v[108:109], v[108:109], v[232:233], v[228:229]
	v_pk_fma_f32 v[106:107], v[106:107], v[230:231], v[226:227]
	global_store_dwordx4 v[128:129], v[106:109], off offset:64
	s_nop 1
	s_waitcnt vmcnt(4)
	v_pk_fma_f32 v[104:105], v[104:105], v[240:241], v[236:237]
	v_pk_fma_f32 v[102:103], v[102:103], v[238:239], v[234:235]
	global_store_dwordx4 v[128:129], v[102:105], off offset:512
	s_nop 1
	v_or_b32_e32 v102, 32, v146
	v_cmp_gt_i32_e32 vcc, s36, v102
	v_cmp_lt_i32_e64 s[4:5], s42, v102
	s_waitcnt vmcnt(3)
	v_pk_fma_f32 v[100:101], v[100:101], v[200:201], v[196:197]
	v_pk_fma_f32 v[98:99], v[98:99], v[198:199], v[194:195]
	global_store_dwordx4 v[128:129], v[98:101], off offset:576
	s_and_saveexec_b64 s[28:29], s[4:5]
	s_xor_b64 s[4:5], exec, s[28:29]
	v_add_u32_e32 v134, 0xffffe020, v146
	v_lshlrev_b64 v[98:99], 13, v[134:135]
	v_mov_b32_e32 v103, v135
	v_lshl_add_u64 v[100:101], s[8:9], 0, v[98:99]
	v_lshlrev_b64 v[98:99], 13, v[102:103]
	s_or_saveexec_b64 s[4:5], s[4:5]
	v_ashrrev_i32_e32 v103, 31, v102
	s_xor_b64 exec, exec, s[4:5]
	s_cbranch_execz .LBB0_1843
	v_readlane_b32 s68, v248, 9
	v_lshlrev_b64 v[98:99], 13, v[102:103]
	v_readlane_b32 s72, v248, 13
	v_readlane_b32 s73, v248, 14
	v_readlane_b32 s69, v248, 10
	v_readlane_b32 s70, v248, 11
	v_lshl_add_u64 v[100:101], s[72:73], 0, v[98:99]
	v_readlane_b32 s71, v248, 12
	v_readlane_b32 s74, v248, 15
	v_readlane_b32 s75, v248, 16
	v_readlane_b32 s76, v248, 17
	v_readlane_b32 s77, v248, 18
	v_readlane_b32 s78, v248, 19
	v_readlane_b32 s79, v248, 20
	v_readlane_b32 s80, v248, 21
	v_readlane_b32 s81, v248, 22
	v_readlane_b32 s82, v248, 23
	v_readlane_b32 s83, v248, 24
;     __device__ __forceinline__ void operator()(const pg8::f32x4 (&acc)[2][2][4][2], const pg8::Unit& u, int wr, int wc, int fr, int fq) const {
;         const int row0 = u.pm * 256 + wr * 64 + fr, col0 = u.pn * 256 + wc * 32 + 4 * fq;
; #pragma unroll
;         for (int ai = 0; ai < 2; ++ai)
; #pragma unroll
;             for (int m = 0; m < 4; ++m) { const int row = row0 + ai * 128 + m * 16;
;                 const float* rp = (row < NL ? res_lat + (size_t)row * DM : res_ctx + (size_t)(row - NL) * DM) + col0;
;                 const float* gp = gate + rowgrp(row) * MODW + col0;
;                 float* cp = C + (size_t)row * DM + col0;
; #pragma unroll
;                 for (int bj = 0; bj < 2; ++bj)
; #pragma unroll
;                     for (int n = 0; n < 2; ++n) { const pg8::f32x4 r = *(const pg8::f32x4*)(rp + bj * 128 + n * 16), g = *(const pg8::f32x4*)(gp + bj * 128 + n * 16);
;                         *(pg8::f32x4*)(cp + bj * 128 + n * 16) = r + g * acc[ai][bj][m][n]; } }
;     }
.LBB0_1843:
	s_or_b64 exec, exec, s[4:5]
	v_lshl_add_u64 v[108:109], v[100:101], 0, v[144:145]
	v_lshrrev_b32_e32 v100, 20, v103
	v_add_u32_e32 v100, v102, v100
	v_ashrrev_i32_e32 v100, 12, v100
	v_mul_i32_i24_e32 v100, 0x3000, v100
	v_cndmask_b32_e32 v100, v158, v100, vcc
	v_ashrrev_i32_e32 v101, 31, v100
	v_lshl_add_u64 v[100:101], v[100:101], 2, s[10:11]
	v_lshl_add_u64 v[110:111], v[100:101], 0, v[144:145]
	global_load_dwordx4 v[100:103], v[108:109], off
	global_load_dwordx4 v[104:107], v[110:111], off
	global_load_dwordx4 v[226:229], v[108:109], off offset:64
	global_load_dwordx4 v[230:233], v[110:111], off offset:64
	global_load_dwordx4 v[234:237], v[108:109], off offset:512
	global_load_dwordx4 v[238:241], v[110:111], off offset:512
	global_load_dwordx4 v[194:197], v[108:109], off offset:576
	global_load_dwordx4 v[198:201], v[110:111], off offset:576
	v_readlane_b32 s68, v248, 9
	v_readlane_b32 s70, v248, 11
	v_readlane_b32 s71, v248, 12
	v_readlane_b32 s69, v248, 10
	v_readlane_b32 s72, v248, 13
	v_lshl_add_u64 v[98:99], s[70:71], 0, v[98:99]
	v_lshl_add_u64 v[112:113], v[98:99], 0, v[144:145]
	v_readlane_b32 s73, v248, 14
	v_readlane_b32 s74, v248, 15
	v_readlane_b32 s75, v248, 16
	v_readlane_b32 s76, v248, 17
	v_readlane_b32 s77, v248, 18
	v_readlane_b32 s78, v248, 19
	v_readlane_b32 s79, v248, 20
	v_readlane_b32 s80, v248, 21
	v_readlane_b32 s81, v248, 22
	v_readlane_b32 s82, v248, 23
	v_readlane_b32 s83, v248, 24
	s_waitcnt vmcnt(6)
	v_pk_fma_f32 v[96:97], v[96:97], v[106:107], v[102:103]
	v_pk_fma_f32 v[94:95], v[94:95], v[104:105], v[100:101]
	global_store_dwordx4 v[112:113], v[94:97], off
	s_nop 1
	s_waitcnt vmcnt(5)
	v_pk_fma_f32 v[92:93], v[92:93], v[232:233], v[228:229]
	v_pk_fma_f32 v[90:91], v[90:91], v[230:231], v[226:227]
	global_store_dwordx4 v[112:113], v[90:93], off offset:64
	s_nop 1
	s_waitcnt vmcnt(4)
	v_pk_fma_f32 v[88:89], v[88:89], v[240:241], v[236:237]
	v_pk_fma_f32 v[86:87], v[86:87], v[238:239], v[234:235]
	global_store_dwordx4 v[112:113], v[86:89], off offset:512
	s_nop 1
	v_or_b32_e32 v86, 48, v146
	v_cmp_gt_i32_e32 vcc, s36, v86
	v_cmp_lt_i32_e64 s[4:5], s42, v86
	s_waitcnt vmcnt(3)
	v_pk_fma_f32 v[84:85], v[84:85], v[200:201], v[196:197]
	v_pk_fma_f32 v[82:83], v[82:83], v[198:199], v[194:195]
	global_store_dwordx4 v[112:113], v[82:85], off offset:576
	s_and_saveexec_b64 s[28:29], s[4:5]
	s_xor_b64 s[4:5], exec, s[28:29]
	v_add_u32_e32 v134, 0xffffe030, v146
	v_lshlrev_b64 v[82:83], 13, v[134:135]
	v_mov_b32_e32 v87, v135
	v_lshl_add_u64 v[84:85], s[8:9], 0, v[82:83]
	v_lshlrev_b64 v[82:83], 13, v[86:87]
	s_or_saveexec_b64 s[4:5], s[4:5]
	v_ashrrev_i32_e32 v87, 31, v86
	s_xor_b64 exec, exec, s[4:5]
	s_cbranch_execz .LBB0_1847
	v_readlane_b32 s68, v248, 9
	v_lshlrev_b64 v[82:83], 13, v[86:87]
	v_readlane_b32 s72, v248, 13
	v_readlane_b32 s73, v248, 14
	v_readlane_b32 s69, v248, 10
	v_readlane_b32 s70, v248, 11
	v_lshl_add_u64 v[84:85], s[72:73], 0, v[82:83]
	v_readlane_b32 s71, v248, 12
	v_readlane_b32 s74, v248, 15
	v_readlane_b32 s75, v248, 16
	v_readlane_b32 s76, v248, 17
	v_readlane_b32 s77, v248, 18
	v_readlane_b32 s78, v248, 19
	v_readlane_b32 s79, v248, 20
	v_readlane_b32 s80, v248, 21
	v_readlane_b32 s81, v248, 22
	v_readlane_b32 s82, v248, 23
	v_readlane_b32 s83, v248, 24
.LBB0_1847:
	s_or_b64 exec, exec, s[4:5]
	v_lshl_add_u64 v[92:93], v[84:85], 0, v[144:145]
	v_lshrrev_b32_e32 v84, 20, v87
	v_add_u32_e32 v84, v86, v84
	v_ashrrev_i32_e32 v84, 12, v84
	v_mul_i32_i24_e32 v84, 0x3000, v84
	v_cndmask_b32_e32 v84, v158, v84, vcc
	v_ashrrev_i32_e32 v85, 31, v84
	v_lshl_add_u64 v[84:85], v[84:85], 2, s[10:11]
	v_lshl_add_u64 v[94:95], v[84:85], 0, v[144:145]
	global_load_dwordx4 v[84:87], v[92:93], off
	global_load_dwordx4 v[88:91], v[94:95], off
	global_load_dwordx4 v[226:229], v[92:93], off offset:64
	global_load_dwordx4 v[230:233], v[94:95], off offset:64
	global_load_dwordx4 v[234:237], v[92:93], off offset:512
	global_load_dwordx4 v[238:241], v[94:95], off offset:512
	global_load_dwordx4 v[194:197], v[92:93], off offset:576
	global_load_dwordx4 v[198:201], v[94:95], off offset:576
	v_readlane_b32 s68, v248, 9
	v_readlane_b32 s70, v248, 11
	v_readlane_b32 s71, v248, 12
	s_movk_i32 s4, 0x1f80
	s_movk_i32 s5, 0x1f7f
	v_lshl_add_u64 v[82:83], s[70:71], 0, v[82:83]
	v_lshl_add_u64 v[96:97], v[82:83], 0, v[144:145]
	v_cmp_gt_i32_e32 vcc, s4, v146
	v_cmp_lt_i32_e64 s[4:5], s5, v146
	v_readlane_b32 s69, v248, 10
	v_readlane_b32 s72, v248, 13
	v_readlane_b32 s73, v248, 14
	v_readlane_b32 s74, v248, 15
	v_readlane_b32 s75, v248, 16
	v_readlane_b32 s76, v248, 17
	v_readlane_b32 s77, v248, 18
	v_readlane_b32 s78, v248, 19
	v_readlane_b32 s79, v248, 20
	v_readlane_b32 s80, v248, 21
	v_readlane_b32 s81, v248, 22
	v_readlane_b32 s82, v248, 23
	v_readlane_b32 s83, v248, 24
	s_waitcnt vmcnt(6)
	v_pk_fma_f32 v[80:81], v[80:81], v[90:91], v[86:87]
	v_pk_fma_f32 v[78:79], v[78:79], v[88:89], v[84:85]
	global_store_dwordx4 v[96:97], v[78:81], off
	s_nop 1
	s_waitcnt vmcnt(5)
	v_pk_fma_f32 v[76:77], v[76:77], v[232:233], v[228:229]
	v_pk_fma_f32 v[74:75], v[74:75], v[230:231], v[226:227]
	global_store_dwordx4 v[96:97], v[74:77], off offset:64
	s_nop 1
	s_waitcnt vmcnt(4)
	v_pk_fma_f32 v[72:73], v[72:73], v[240:241], v[236:237]
	v_pk_fma_f32 v[70:71], v[70:71], v[238:239], v[234:235]
	global_store_dwordx4 v[96:97], v[70:73], off offset:512
	s_nop 1
	v_add_u32_e32 v70, 0x80, v146
	s_waitcnt vmcnt(3)
	v_pk_fma_f32 v[68:69], v[68:69], v[200:201], v[196:197]
	v_pk_fma_f32 v[66:67], v[66:67], v[198:199], v[194:195]
	global_store_dwordx4 v[96:97], v[66:69], off offset:576
	s_and_saveexec_b64 s[28:29], s[4:5]
	s_xor_b64 s[4:5], exec, s[28:29]
	v_add_u32_e32 v134, 0xffffe080, v146
	v_lshlrev_b64 v[66:67], 13, v[134:135]
	v_mov_b32_e32 v71, v135
	v_lshl_add_u64 v[68:69], s[8:9], 0, v[66:67]
	v_lshlrev_b64 v[66:67], 13, v[70:71]
	s_or_saveexec_b64 s[4:5], s[4:5]
	v_ashrrev_i32_e32 v71, 31, v70
	s_xor_b64 exec, exec, s[4:5]
	s_cbranch_execz .LBB0_1851
	v_readlane_b32 s68, v248, 9
	v_lshlrev_b64 v[66:67], 13, v[70:71]
	v_readlane_b32 s72, v248, 13
	v_readlane_b32 s73, v248, 14
	v_readlane_b32 s69, v248, 10
	v_readlane_b32 s70, v248, 11
	v_lshl_add_u64 v[68:69], s[72:73], 0, v[66:67]
	v_readlane_b32 s71, v248, 12
	v_readlane_b32 s74, v248, 15
	v_readlane_b32 s75, v248, 16
	v_readlane_b32 s76, v248, 17
	v_readlane_b32 s77, v248, 18
	v_readlane_b32 s78, v248, 19
	v_readlane_b32 s79, v248, 20
	v_readlane_b32 s80, v248, 21
	v_readlane_b32 s81, v248, 22
	v_readlane_b32 s82, v248, 23
	v_readlane_b32 s83, v248, 24
;     __device__ __forceinline__ void operator()(const pg8::f32x4 (&acc)[2][2][4][2], const pg8::Unit& u, int wr, int wc, int fr, int fq) const {
;         const int row0 = u.pm * 256 + wr * 64 + fr, col0 = u.pn * 256 + wc * 32 + 4 * fq;
; #pragma unroll
;         for (int ai = 0; ai < 2; ++ai)
; #pragma unroll
;             for (int m = 0; m < 4; ++m) { const int row = row0 + ai * 128 + m * 16;
;                 const float* rp = (row < NL ? res_lat + (size_t)row * DM : res_ctx + (size_t)(row - NL) * DM) + col0;
;                 const float* gp = gate + rowgrp(row) * MODW + col0;
;                 float* cp = C + (size_t)row * DM + col0;
; #pragma unroll
;                 for (int bj = 0; bj < 2; ++bj)
; #pragma unroll
;                     for (int n = 0; n < 2; ++n) { const pg8::f32x4 r = *(const pg8::f32x4*)(rp + bj * 128 + n * 16), g = *(const pg8::f32x4*)(gp + bj * 128 + n * 16);
;                         *(pg8::f32x4*)(cp + bj * 128 + n * 16) = r + g * acc[ai][bj][m][n]; } }
;     }
.LBB0_1851:
	s_or_b64 exec, exec, s[4:5]
	v_lshl_add_u64 v[76:77], v[68:69], 0, v[144:145]
	v_lshrrev_b32_e32 v68, 20, v71
	v_add_u32_e32 v68, v70, v68
	v_ashrrev_i32_e32 v68, 12, v68
	v_mul_i32_i24_e32 v68, 0x3000, v68
	v_cndmask_b32_e32 v68, v158, v68, vcc
	v_ashrrev_i32_e32 v69, 31, v68
	v_lshl_add_u64 v[68:69], v[68:69], 2, s[10:11]
	v_lshl_add_u64 v[78:79], v[68:69], 0, v[144:145]
	global_load_dwordx4 v[68:71], v[76:77], off
	global_load_dwordx4 v[72:75], v[78:79], off
	global_load_dwordx4 v[226:229], v[76:77], off offset:64
	global_load_dwordx4 v[230:233], v[78:79], off offset:64
	global_load_dwordx4 v[234:237], v[76:77], off offset:512
	global_load_dwordx4 v[238:241], v[78:79], off offset:512
	global_load_dwordx4 v[194:197], v[76:77], off offset:576
	global_load_dwordx4 v[198:201], v[78:79], off offset:576
	v_readlane_b32 s68, v248, 9
	v_readlane_b32 s70, v248, 11
	v_readlane_b32 s71, v248, 12
	s_movk_i32 s4, 0x1f70
	s_movk_i32 s5, 0x1f6f
	v_lshl_add_u64 v[66:67], s[70:71], 0, v[66:67]
	v_lshl_add_u64 v[80:81], v[66:67], 0, v[144:145]
	v_cmp_gt_i32_e32 vcc, s4, v146
	v_cmp_lt_i32_e64 s[4:5], s5, v146
	v_readlane_b32 s69, v248, 10
	v_readlane_b32 s72, v248, 13
	v_readlane_b32 s73, v248, 14
	v_readlane_b32 s74, v248, 15
	v_readlane_b32 s75, v248, 16
	v_readlane_b32 s76, v248, 17
	v_readlane_b32 s77, v248, 18
	v_readlane_b32 s78, v248, 19
	v_readlane_b32 s79, v248, 20
	v_readlane_b32 s80, v248, 21
	v_readlane_b32 s81, v248, 22
	v_readlane_b32 s82, v248, 23
	v_readlane_b32 s83, v248, 24
	s_waitcnt vmcnt(6)
	v_pk_fma_f32 v[64:65], v[64:65], v[74:75], v[70:71]
	v_pk_fma_f32 v[62:63], v[62:63], v[72:73], v[68:69]
	global_store_dwordx4 v[80:81], v[62:65], off
	s_nop 1
	s_waitcnt vmcnt(5)
	v_pk_fma_f32 v[60:61], v[60:61], v[232:233], v[228:229]
	v_pk_fma_f32 v[58:59], v[58:59], v[230:231], v[226:227]
	global_store_dwordx4 v[80:81], v[58:61], off offset:64
	s_nop 1
	s_waitcnt vmcnt(4)
	v_pk_fma_f32 v[56:57], v[56:57], v[240:241], v[236:237]
	v_pk_fma_f32 v[54:55], v[54:55], v[238:239], v[234:235]
	global_store_dwordx4 v[80:81], v[54:57], off offset:512
	s_nop 1
	v_add_u32_e32 v54, 0x90, v146
	s_waitcnt vmcnt(3)
	v_pk_fma_f32 v[52:53], v[52:53], v[200:201], v[196:197]
	v_pk_fma_f32 v[50:51], v[50:51], v[198:199], v[194:195]
	global_store_dwordx4 v[80:81], v[50:53], off offset:576
	s_and_saveexec_b64 s[28:29], s[4:5]
	s_xor_b64 s[4:5], exec, s[28:29]
	v_add_u32_e32 v134, 0xffffe090, v146
	v_lshlrev_b64 v[50:51], 13, v[134:135]
	v_mov_b32_e32 v55, v135
	v_lshl_add_u64 v[52:53], s[8:9], 0, v[50:51]
	v_lshlrev_b64 v[50:51], 13, v[54:55]
	s_or_saveexec_b64 s[4:5], s[4:5]
	v_ashrrev_i32_e32 v55, 31, v54
	s_xor_b64 exec, exec, s[4:5]
	s_cbranch_execz .LBB0_1855
	v_readlane_b32 s68, v248, 9
	v_lshlrev_b64 v[50:51], 13, v[54:55]
	v_readlane_b32 s72, v248, 13
	v_readlane_b32 s73, v248, 14
	v_readlane_b32 s69, v248, 10
	v_readlane_b32 s70, v248, 11
	v_lshl_add_u64 v[52:53], s[72:73], 0, v[50:51]
	v_readlane_b32 s71, v248, 12
	v_readlane_b32 s74, v248, 15
	v_readlane_b32 s75, v248, 16
	v_readlane_b32 s76, v248, 17
	v_readlane_b32 s77, v248, 18
	v_readlane_b32 s78, v248, 19
	v_readlane_b32 s79, v248, 20
	v_readlane_b32 s80, v248, 21
	v_readlane_b32 s81, v248, 22
	v_readlane_b32 s82, v248, 23
	v_readlane_b32 s83, v248, 24
.LBB0_1855:
	s_or_b64 exec, exec, s[4:5]
	v_lshl_add_u64 v[60:61], v[52:53], 0, v[144:145]
	v_lshrrev_b32_e32 v52, 20, v55
	v_add_u32_e32 v52, v54, v52
	v_ashrrev_i32_e32 v52, 12, v52
	v_mul_i32_i24_e32 v52, 0x3000, v52
	v_cndmask_b32_e32 v52, v158, v52, vcc
	v_ashrrev_i32_e32 v53, 31, v52
	v_lshl_add_u64 v[52:53], v[52:53], 2, s[10:11]
	v_lshl_add_u64 v[62:63], v[52:53], 0, v[144:145]
	global_load_dwordx4 v[52:55], v[60:61], off
	global_load_dwordx4 v[56:59], v[62:63], off
	global_load_dwordx4 v[226:229], v[60:61], off offset:64
	global_load_dwordx4 v[230:233], v[62:63], off offset:64
	global_load_dwordx4 v[234:237], v[60:61], off offset:512
	global_load_dwordx4 v[238:241], v[62:63], off offset:512
	global_load_dwordx4 v[194:197], v[60:61], off offset:576
	global_load_dwordx4 v[198:201], v[62:63], off offset:576
	v_readlane_b32 s68, v248, 9
	v_readlane_b32 s70, v248, 11
	v_readlane_b32 s71, v248, 12
	s_movk_i32 s4, 0x1f60
	s_movk_i32 s5, 0x1f5f
	v_lshl_add_u64 v[50:51], s[70:71], 0, v[50:51]
	v_lshl_add_u64 v[64:65], v[50:51], 0, v[144:145]
	v_cmp_gt_i32_e32 vcc, s4, v146
	v_cmp_lt_i32_e64 s[4:5], s5, v146
	v_readlane_b32 s69, v248, 10
	v_readlane_b32 s72, v248, 13
	v_readlane_b32 s73, v248, 14
	v_readlane_b32 s74, v248, 15
	v_readlane_b32 s75, v248, 16
	v_readlane_b32 s76, v248, 17
	v_readlane_b32 s77, v248, 18
	v_readlane_b32 s78, v248, 19
	v_readlane_b32 s79, v248, 20
	v_readlane_b32 s80, v248, 21
	v_readlane_b32 s81, v248, 22
	v_readlane_b32 s82, v248, 23
	v_readlane_b32 s83, v248, 24
	s_waitcnt vmcnt(6)
	v_pk_fma_f32 v[48:49], v[48:49], v[58:59], v[54:55]
	v_pk_fma_f32 v[46:47], v[46:47], v[56:57], v[52:53]
	global_store_dwordx4 v[64:65], v[46:49], off
	s_nop 1
	s_waitcnt vmcnt(5)
	v_pk_fma_f32 v[44:45], v[44:45], v[232:233], v[228:229]
	v_pk_fma_f32 v[42:43], v[42:43], v[230:231], v[226:227]
	global_store_dwordx4 v[64:65], v[42:45], off offset:64
	s_nop 1
	s_waitcnt vmcnt(4)
	v_pk_fma_f32 v[40:41], v[40:41], v[240:241], v[236:237]
	v_pk_fma_f32 v[38:39], v[38:39], v[238:239], v[234:235]
	global_store_dwordx4 v[64:65], v[38:41], off offset:512
	s_nop 1
	v_add_u32_e32 v38, 0xa0, v146
	s_waitcnt vmcnt(3)
	v_pk_fma_f32 v[36:37], v[36:37], v[200:201], v[196:197]
	v_pk_fma_f32 v[34:35], v[34:35], v[198:199], v[194:195]
	global_store_dwordx4 v[64:65], v[34:37], off offset:576
	s_and_saveexec_b64 s[28:29], s[4:5]
	s_xor_b64 s[4:5], exec, s[28:29]
	v_add_u32_e32 v134, 0xffffe0a0, v146
	v_lshlrev_b64 v[34:35], 13, v[134:135]
	v_mov_b32_e32 v39, v135
	v_lshl_add_u64 v[36:37], s[8:9], 0, v[34:35]
	v_lshlrev_b64 v[34:35], 13, v[38:39]
	s_or_saveexec_b64 s[4:5], s[4:5]
	v_ashrrev_i32_e32 v39, 31, v38
	s_xor_b64 exec, exec, s[4:5]
	s_cbranch_execz .LBB0_1859
	v_readlane_b32 s68, v248, 9
	v_lshlrev_b64 v[34:35], 13, v[38:39]
	v_readlane_b32 s72, v248, 13
	v_readlane_b32 s73, v248, 14
	v_readlane_b32 s69, v248, 10
	v_readlane_b32 s70, v248, 11
	v_lshl_add_u64 v[36:37], s[72:73], 0, v[34:35]
	v_readlane_b32 s71, v248, 12
	v_readlane_b32 s74, v248, 15
	v_readlane_b32 s75, v248, 16
	v_readlane_b32 s76, v248, 17
	v_readlane_b32 s77, v248, 18
	v_readlane_b32 s78, v248, 19
	v_readlane_b32 s79, v248, 20
	v_readlane_b32 s80, v248, 21
	v_readlane_b32 s81, v248, 22
	v_readlane_b32 s82, v248, 23
	v_readlane_b32 s83, v248, 24
;     __device__ __forceinline__ void operator()(const pg8::f32x4 (&acc)[2][2][4][2], const pg8::Unit& u, int wr, int wc, int fr, int fq) const {
;         const int row0 = u.pm * 256 + wr * 64 + fr, col0 = u.pn * 256 + wc * 32 + 4 * fq;
; #pragma unroll
;         for (int ai = 0; ai < 2; ++ai)
; #pragma unroll
;             for (int m = 0; m < 4; ++m) { const int row = row0 + ai * 128 + m * 16;
;                 const float* rp = (row < NL ? res_lat + (size_t)row * DM : res_ctx + (size_t)(row - NL) * DM) + col0;
;                 const float* gp = gate + rowgrp(row) * MODW + col0;
;                 float* cp = C + (size_t)row * DM + col0;
; #pragma unroll
;                 for (int bj = 0; bj < 2; ++bj)
; #pragma unroll
;                     for (int n = 0; n < 2; ++n) { const pg8::f32x4 r = *(const pg8::f32x4*)(rp + bj * 128 + n * 16), g = *(const pg8::f32x4*)(gp + bj * 128 + n * 16);
;                         *(pg8::f32x4*)(cp + bj * 128 + n * 16) = r + g * acc[ai][bj][m][n]; } }
;     }
.LBB0_1859:
	s_or_b64 exec, exec, s[4:5]
	v_lshl_add_u64 v[44:45], v[36:37], 0, v[144:145]
	v_lshrrev_b32_e32 v36, 20, v39
	v_add_u32_e32 v36, v38, v36
	v_ashrrev_i32_e32 v36, 12, v36
	v_mul_i32_i24_e32 v36, 0x3000, v36
	v_cndmask_b32_e32 v36, v158, v36, vcc
	v_ashrrev_i32_e32 v37, 31, v36
	v_lshl_add_u64 v[36:37], v[36:37], 2, s[10:11]
	v_lshl_add_u64 v[46:47], v[36:37], 0, v[144:145]
	global_load_dwordx4 v[36:39], v[44:45], off
	global_load_dwordx4 v[40:43], v[46:47], off
	global_load_dwordx4 v[226:229], v[44:45], off offset:64
	global_load_dwordx4 v[230:233], v[46:47], off offset:64
	global_load_dwordx4 v[234:237], v[44:45], off offset:512
	global_load_dwordx4 v[238:241], v[46:47], off offset:512
	global_load_dwordx4 v[194:197], v[44:45], off offset:576
	global_load_dwordx4 v[198:201], v[46:47], off offset:576
	v_readlane_b32 s68, v248, 9
	v_readlane_b32 s70, v248, 11
	v_readlane_b32 s71, v248, 12
	s_movk_i32 s4, 0x1f50
	s_movk_i32 s5, 0x1f4f
	v_lshl_add_u64 v[34:35], s[70:71], 0, v[34:35]
	v_lshl_add_u64 v[48:49], v[34:35], 0, v[144:145]
	v_cmp_gt_i32_e32 vcc, s4, v146
	v_cmp_lt_i32_e64 s[4:5], s5, v146
	v_readlane_b32 s69, v248, 10
	v_readlane_b32 s72, v248, 13
	v_readlane_b32 s73, v248, 14
	v_readlane_b32 s74, v248, 15
	v_readlane_b32 s75, v248, 16
	v_readlane_b32 s76, v248, 17
	v_readlane_b32 s77, v248, 18
	v_readlane_b32 s78, v248, 19
	v_readlane_b32 s79, v248, 20
	v_readlane_b32 s80, v248, 21
	v_readlane_b32 s81, v248, 22
	v_readlane_b32 s82, v248, 23
	v_readlane_b32 s83, v248, 24
	s_waitcnt vmcnt(6)
	v_pk_fma_f32 v[32:33], v[32:33], v[42:43], v[38:39]
	v_pk_fma_f32 v[30:31], v[30:31], v[40:41], v[36:37]
	global_store_dwordx4 v[48:49], v[30:33], off
	s_nop 1
	s_waitcnt vmcnt(5)
	v_pk_fma_f32 v[28:29], v[28:29], v[232:233], v[228:229]
	v_pk_fma_f32 v[26:27], v[26:27], v[230:231], v[226:227]
	global_store_dwordx4 v[48:49], v[26:29], off offset:64
	s_nop 1
	s_waitcnt vmcnt(4)
	v_pk_fma_f32 v[24:25], v[24:25], v[240:241], v[236:237]
	v_pk_fma_f32 v[22:23], v[22:23], v[238:239], v[234:235]
	global_store_dwordx4 v[48:49], v[22:25], off offset:512
	s_nop 1
	v_add_u32_e32 v22, 0xb0, v146
	s_waitcnt vmcnt(3)
	v_pk_fma_f32 v[20:21], v[20:21], v[200:201], v[196:197]
	v_pk_fma_f32 v[18:19], v[18:19], v[198:199], v[194:195]
	global_store_dwordx4 v[48:49], v[18:21], off offset:576
	s_and_saveexec_b64 s[28:29], s[4:5]
	s_xor_b64 s[4:5], exec, s[28:29]
	v_add_u32_e32 v134, 0xffffe0b0, v146
	v_lshlrev_b64 v[18:19], 13, v[134:135]
	v_mov_b32_e32 v23, v135
	v_lshl_add_u64 v[20:21], s[8:9], 0, v[18:19]
	v_lshlrev_b64 v[18:19], 13, v[22:23]
	s_or_saveexec_b64 s[4:5], s[4:5]
	v_ashrrev_i32_e32 v23, 31, v22
	s_xor_b64 exec, exec, s[4:5]
	s_cbranch_execz .LBB0_1863
	v_readlane_b32 s68, v248, 9
	v_lshlrev_b64 v[18:19], 13, v[22:23]
	v_readlane_b32 s72, v248, 13
	v_readlane_b32 s73, v248, 14
	v_readlane_b32 s69, v248, 10
	v_readlane_b32 s70, v248, 11
	v_lshl_add_u64 v[20:21], s[72:73], 0, v[18:19]
	v_readlane_b32 s71, v248, 12
	v_readlane_b32 s74, v248, 15
	v_readlane_b32 s75, v248, 16
	v_readlane_b32 s76, v248, 17
	v_readlane_b32 s77, v248, 18
	v_readlane_b32 s78, v248, 19
	v_readlane_b32 s79, v248, 20
	v_readlane_b32 s80, v248, 21
	v_readlane_b32 s81, v248, 22
	v_readlane_b32 s82, v248, 23
	v_readlane_b32 s83, v248, 24
.LBB0_1863:
	s_or_b64 exec, exec, s[4:5]
	v_lshl_add_u64 v[28:29], v[20:21], 0, v[144:145]
	v_lshrrev_b32_e32 v20, 20, v23
	v_add_u32_e32 v20, v22, v20
	v_ashrrev_i32_e32 v20, 12, v20
	v_mul_i32_i24_e32 v20, 0x3000, v20
	v_cndmask_b32_e32 v20, v158, v20, vcc
	v_ashrrev_i32_e32 v21, 31, v20
	v_lshl_add_u64 v[20:21], v[20:21], 2, s[10:11]
	v_lshl_add_u64 v[30:31], v[20:21], 0, v[144:145]
	global_load_dwordx4 v[20:23], v[28:29], off
	global_load_dwordx4 v[24:27], v[30:31], off
	global_load_dwordx4 v[226:229], v[28:29], off offset:64
	global_load_dwordx4 v[230:233], v[30:31], off offset:64
	global_load_dwordx4 v[234:237], v[28:29], off offset:512
	global_load_dwordx4 v[238:241], v[30:31], off offset:512
	global_load_dwordx4 v[194:197], v[28:29], off offset:576
	global_load_dwordx4 v[198:201], v[30:31], off offset:576
	v_readlane_b32 s68, v248, 9
	v_readlane_b32 s70, v248, 11
	v_readlane_b32 s71, v248, 12
	s_andn2_b64 vcc, exec, s[0:1]
	s_mov_b64 s[0:1], -1
	v_lshl_add_u64 v[18:19], s[70:71], 0, v[18:19]
	v_lshl_add_u64 v[32:33], v[18:19], 0, v[144:145]
	v_readlane_b32 s69, v248, 10
	v_readlane_b32 s72, v248, 13
	v_readlane_b32 s73, v248, 14
	v_readlane_b32 s74, v248, 15
	v_readlane_b32 s75, v248, 16
	v_readlane_b32 s76, v248, 17
	v_readlane_b32 s77, v248, 18
	v_readlane_b32 s78, v248, 19
	v_readlane_b32 s79, v248, 20
	v_readlane_b32 s80, v248, 21
	v_readlane_b32 s81, v248, 22
	v_readlane_b32 s82, v248, 23
	v_readlane_b32 s83, v248, 24
	s_waitcnt vmcnt(6)
	v_pk_fma_f32 v[16:17], v[16:17], v[26:27], v[22:23]
	v_pk_fma_f32 v[14:15], v[14:15], v[24:25], v[20:21]
	global_store_dwordx4 v[32:33], v[14:17], off
	s_nop 1
	s_waitcnt vmcnt(5)
	v_pk_fma_f32 v[12:13], v[12:13], v[232:233], v[228:229]
	v_pk_fma_f32 v[10:11], v[10:11], v[230:231], v[226:227]
	global_store_dwordx4 v[32:33], v[10:13], off offset:64
	s_nop 1
	s_waitcnt vmcnt(4)
	v_pk_fma_f32 v[8:9], v[8:9], v[240:241], v[236:237]
	v_pk_fma_f32 v[6:7], v[6:7], v[238:239], v[234:235]
	global_store_dwordx4 v[32:33], v[6:9], off offset:512
	s_nop 1
	s_waitcnt vmcnt(3)
	v_pk_fma_f32 v[4:5], v[4:5], v[200:201], v[196:197]
	v_pk_fma_f32 v[2:3], v[2:3], v[198:199], v[194:195]
	global_store_dwordx4 v[32:33], v[2:5], off offset:576
	s_cbranch_vccnz .LBB0_1820
	s_andn2_b64 vcc, exec, s[6:7]
	s_cbranch_vccnz .LBB0_1819
	s_barrier
	s_branch .LBB0_1819
